# cache policy: nt on both the once-read f32 weight loads and the once-written fp8 weight stores of the conversion units
# speedup vs baseline: 1.0095x; 1.0047x over previous
; #define LAS __attribute__((address_space(3)))
; #define LDS_WAIT() asm volatile("s_waitcnt lgkmcnt(0)" ::: "memory")
; __device__ __forceinline__ void p0_transpose_item8(const float* W, int ldw, int srccol0, int k0, unsigned char* dst, int K, LAS float* scr, int lane) {
;     ...
;     LDS_WAIT(); asm volatile("" ::: "memory");
;     const int c = lane & 7;
; #pragma unroll
;     for (int j = 0; j < 4; ++j) { const int n = (lane >> 3) + 8 * j; const LAS float* s = scr + (8 * c) * 33 + n;
;         u32x2 o; o.x = pk4_f8(s[0 * 33] * 32.f, s[1 * 33] * 32.f, s[2 * 33] * 32.f, s[3 * 33] * 32.f); o.y = pk4_f8(s[4 * 33] * 32.f, s[5 * 33] * 32.f, s[6 * 33] * 32.f, s[7 * 33] * 32.f);
;         *(u32x2*)(dst + (size_t)n * K + k0 + 8 * c) = o; }
;     LDS_WAIT(); asm volatile("" ::: "memory");
; __device__ __forceinline__ void p0_item(KP Pk, Frame& F, int it, LAS float* scr) {
;     ...
;     { const int le = it / TI_DN, r = it % TI_DN, kb = r / 64, nb = r % 64;
;         p0_transpose_item8(Pk->in[I_ED] + (size_t)le * DE * D, D, 32 * nb, 64 * kb, ws + WS_WD + ((size_t)le * D + 32 * nb) * DE, DE, scr, F.lane); }
.Lcv_dn_0_n:
	ds_read2_b32 v[34:35], v50 offset1:8
	ds_read2_b32 v[36:37], v50 offset0:33 offset1:41
	ds_read2_b32 v[44:45], v50 offset0:132 offset1:140
	ds_read2_b32 v[46:47], v50 offset0:165 offset1:173
	ds_read2_b32 v[38:39], v50 offset0:66 offset1:74
	ds_read2_b32 v[40:41], v50 offset0:99 offset1:107
	s_waitcnt lgkmcnt(5)
	v_mul_f32_e32 v3, 0x42000000, v34
	s_waitcnt lgkmcnt(4)
	v_mul_f32_e32 v34, 0x42000000, v36
	v_med3_f32 v3, v3, s83, v238
	v_med3_f32 v34, v34, s83, v238
	ds_read2_b32 v[48:49], v50 offset0:198 offset1:206
	ds_read2_b32 v[52:53], v50 offset0:231 offset1:239
	v_cvt_pk_fp8_f32 v42, v3, v34
	s_waitcnt lgkmcnt(5)
	v_mul_f32_e32 v3, 0x42000000, v44
	s_waitcnt lgkmcnt(4)
	v_mul_f32_e32 v34, 0x42000000, v46
	v_med3_f32 v3, v3, s83, v238
	v_med3_f32 v34, v34, s83, v238
	s_waitcnt lgkmcnt(3)
	v_mul_f32_e32 v36, 0x42000000, v38
	s_waitcnt lgkmcnt(2)
	v_mul_f32_e32 v38, 0x42000000, v40
	v_cvt_pk_fp8_f32 v43, v3, v34
	v_mul_f32_e32 v3, 0x42000000, v35
	v_mul_f32_e32 v34, 0x42000000, v37
	v_med3_f32 v36, v36, s83, v238
	v_med3_f32 v38, v38, s83, v238
	v_med3_f32 v3, v3, s83, v238
	v_med3_f32 v37, v34, s83, v238
	v_mov_b32_e32 v34, v0
	v_cvt_pk_fp8_f32 v42, v36, v38 op_sel:[0,0,1]
	s_waitcnt lgkmcnt(1)
	v_mul_f32_e32 v36, 0x42000000, v48
	s_waitcnt lgkmcnt(0)
	v_mul_f32_e32 v38, 0x42000000, v52
	v_cvt_pk_fp8_f32 v34, v3, v37
	v_med3_f32 v36, v36, s83, v238
	v_med3_f32 v38, v38, s83, v238
	v_cvt_pk_fp8_f32 v43, v36, v38 op_sel:[0,0,1]
	v_mul_f32_e32 v35, 0x42000000, v39
	v_mul_f32_e32 v36, 0x42000000, v41
	v_med3_f32 v35, v35, s83, v238
	v_med3_f32 v36, v36, s83, v238
	v_cvt_pk_fp8_f32 v34, v35, v36 op_sel:[0,0,1]
	v_mul_f32_e32 v3, 0x42000000, v45
	v_mul_f32_e32 v35, 0x42000000, v47
	v_med3_f32 v3, v3, s83, v238
	v_med3_f32 v38, v35, s83, v238
	v_mov_b32_e32 v35, v0
	v_cvt_pk_fp8_f32 v35, v3, v38
	v_mul_f32_e32 v36, 0x42000000, v49
	v_mul_f32_e32 v37, 0x42000000, v53
	v_med3_f32 v36, v36, s83, v238
	v_med3_f32 v37, v37, s83, v238
	v_cvt_pk_fp8_f32 v35, v36, v37 op_sel:[0,0,1]
	v_lshl_add_u64 v[32:33], s[8:9], 0, v[6:7]
	v_lshl_add_u64 v[36:37], v[32:33], 0, v[10:11]
	ds_read2_b32 v[44:45], v50 offset0:148 offset1:156
	global_store_dwordx2 v[36:37], v[34:35], off nt
	ds_read2_b32 v[34:35], v50 offset0:16 offset1:24
	ds_read2_b32 v[36:37], v50 offset0:49 offset1:57
	ds_read2_b32 v[46:47], v50 offset0:181 offset1:189
	ds_read2_b32 v[38:39], v50 offset0:82 offset1:90
	ds_read2_b32 v[40:41], v50 offset0:115 offset1:123
	v_lshl_add_u64 v[54:55], v[32:33], 0, v[8:9]
	s_waitcnt lgkmcnt(4)
	v_mul_f32_e32 v3, 0x42000000, v34
	s_waitcnt lgkmcnt(3)
	v_mul_f32_e32 v34, 0x42000000, v36
	global_store_dwordx2 v[54:55], v[42:43], off nt
	v_med3_f32 v3, v3, s83, v238
	v_med3_f32 v34, v34, s83, v238
	v_mov_b32_e32 v42, v0
	ds_read2_b32 v[48:49], v50 offset0:214 offset1:222
	ds_read2_b32 v[52:53], v50 offset0:247 offset1:255
	v_cvt_pk_fp8_f32 v42, v3, v34
	v_mul_f32_e32 v3, 0x42000000, v44
	s_waitcnt lgkmcnt(4)
	v_mul_f32_e32 v34, 0x42000000, v46
	v_med3_f32 v3, v3, s83, v238
	v_med3_f32 v34, v34, s83, v238
	v_mov_b32_e32 v43, v0
	s_waitcnt lgkmcnt(3)
	v_mul_f32_e32 v36, 0x42000000, v38
	s_waitcnt lgkmcnt(2)
	v_mul_f32_e32 v38, 0x42000000, v40
	v_cvt_pk_fp8_f32 v43, v3, v34
	v_mul_f32_e32 v3, 0x42000000, v35
	v_mul_f32_e32 v34, 0x42000000, v37
	v_med3_f32 v36, v36, s83, v238
	v_med3_f32 v38, v38, s83, v238
	v_med3_f32 v3, v3, s83, v238
	v_med3_f32 v37, v34, s83, v238
	v_mov_b32_e32 v34, v0
	v_cvt_pk_fp8_f32 v42, v36, v38 op_sel:[0,0,1]
	s_waitcnt lgkmcnt(1)
	v_mul_f32_e32 v36, 0x42000000, v48
	s_waitcnt lgkmcnt(0)
	v_mul_f32_e32 v38, 0x42000000, v52
	v_cvt_pk_fp8_f32 v34, v3, v37
	v_med3_f32 v36, v36, s83, v238
	v_med3_f32 v38, v38, s83, v238
	v_cvt_pk_fp8_f32 v43, v36, v38 op_sel:[0,0,1]
	v_mul_f32_e32 v35, 0x42000000, v39
	v_mul_f32_e32 v36, 0x42000000, v41
	v_med3_f32 v35, v35, s83, v238
	v_med3_f32 v36, v36, s83, v238
	v_cvt_pk_fp8_f32 v34, v35, v36 op_sel:[0,0,1]
	v_mul_f32_e32 v3, 0x42000000, v45
	v_mul_f32_e32 v35, 0x42000000, v47
	v_med3_f32 v3, v3, s83, v238
	v_med3_f32 v38, v35, s83, v238
	v_mov_b32_e32 v35, v0
	v_cvt_pk_fp8_f32 v35, v3, v38
	v_mul_f32_e32 v36, 0x42000000, v49
	v_mul_f32_e32 v37, 0x42000000, v53
	v_med3_f32 v36, v36, s83, v238
	v_med3_f32 v37, v37, s83, v238
	v_cvt_pk_fp8_f32 v35, v36, v37 op_sel:[0,0,1]
	v_lshl_add_u64 v[54:55], v[32:33], 0, v[12:13]
	v_lshl_add_u64 v[32:33], v[32:33], 0, v[14:15]
	global_store_dwordx2 v[54:55], v[42:43], off nt
	global_store_dwordx2 v[32:33], v[34:35], off nt
	s_waitcnt lgkmcnt(0)
	s_add_u32 s8, s8, 0x8000
	s_addc_u32 s9, s9, 0
	s_cmp_eq_u32 s43, 0
	s_cbranch_scc1 .Lcv_dn_1_f
	s_cmp_eq_u32 s43, 12
	s_cbranch_scc1 .Lcv_dn_1_l
	s_waitcnt vmcnt(40)
	s_branch .Lcv_dn_1_d

; #define LAS __attribute__((address_space(3)))
; __device__ __forceinline__ void p0_transpose_item8(const float* W, int ldw, int srccol0, int k0, unsigned char* dst, int K, LAS float* scr, int lane) {
;     ...
;     const int c = lane & 7;
; #pragma unroll
;     for (int j = 0; j < 4; ++j) { const int n = (lane >> 3) + 8 * j; const LAS float* s = scr + (8 * c) * 33 + n;
;         u32x2 o; o.x = pk4_f8(s[0 * 33] * 32.f, s[1 * 33] * 32.f, s[2 * 33] * 32.f, s[3 * 33] * 32.f); o.y = pk4_f8(s[4 * 33] * 32.f, s[5 * 33] * 32.f, s[6 * 33] * 32.f, s[7 * 33] * 32.f);
;         *(u32x2*)(dst + (size_t)n * K + k0 + 8 * c) = o; }
.Lcv_dn_3_n:
	ds_read2_b32 v[34:35], v50 offset1:8
	ds_read2_b32 v[36:37], v50 offset0:33 offset1:41
	ds_read2_b32 v[44:45], v50 offset0:132 offset1:140
	ds_read2_b32 v[46:47], v50 offset0:165 offset1:173
	ds_read2_b32 v[38:39], v50 offset0:66 offset1:74
	ds_read2_b32 v[40:41], v50 offset0:99 offset1:107
	s_waitcnt lgkmcnt(5)
	v_mul_f32_e32 v3, 0x42000000, v34
	s_waitcnt lgkmcnt(4)
	v_mul_f32_e32 v34, 0x42000000, v36
	v_med3_f32 v3, v3, s83, v238
	v_med3_f32 v34, v34, s83, v238
	ds_read2_b32 v[48:49], v50 offset0:198 offset1:206
	ds_read2_b32 v[52:53], v50 offset0:231 offset1:239
	v_cvt_pk_fp8_f32 v42, v3, v34
	s_waitcnt lgkmcnt(5)
	v_mul_f32_e32 v3, 0x42000000, v44
	s_waitcnt lgkmcnt(4)
	v_mul_f32_e32 v34, 0x42000000, v46
	v_med3_f32 v3, v3, s83, v238
	v_med3_f32 v34, v34, s83, v238
	s_waitcnt lgkmcnt(3)
	v_mul_f32_e32 v36, 0x42000000, v38
	s_waitcnt lgkmcnt(2)
	v_mul_f32_e32 v38, 0x42000000, v40
	v_cvt_pk_fp8_f32 v43, v3, v34
	v_mul_f32_e32 v3, 0x42000000, v35
	v_mul_f32_e32 v34, 0x42000000, v37
	v_med3_f32 v36, v36, s83, v238
	v_med3_f32 v38, v38, s83, v238
	v_med3_f32 v3, v3, s83, v238
	v_med3_f32 v37, v34, s83, v238
	v_mov_b32_e32 v34, v0
	v_cvt_pk_fp8_f32 v42, v36, v38 op_sel:[0,0,1]
	s_waitcnt lgkmcnt(1)
	v_mul_f32_e32 v36, 0x42000000, v48
	s_waitcnt lgkmcnt(0)
	v_mul_f32_e32 v38, 0x42000000, v52
	v_cvt_pk_fp8_f32 v34, v3, v37
	v_med3_f32 v36, v36, s83, v238
	v_med3_f32 v38, v38, s83, v238
	v_cvt_pk_fp8_f32 v43, v36, v38 op_sel:[0,0,1]
	v_mul_f32_e32 v35, 0x42000000, v39
	v_mul_f32_e32 v36, 0x42000000, v41
	v_med3_f32 v35, v35, s83, v238
	v_med3_f32 v36, v36, s83, v238
	v_cvt_pk_fp8_f32 v34, v35, v36 op_sel:[0,0,1]
	v_mul_f32_e32 v3, 0x42000000, v45
	v_mul_f32_e32 v35, 0x42000000, v47
	v_med3_f32 v3, v3, s83, v238
	v_med3_f32 v38, v35, s83, v238
	v_mov_b32_e32 v35, v0
	v_cvt_pk_fp8_f32 v35, v3, v38
	v_mul_f32_e32 v36, 0x42000000, v49
	v_mul_f32_e32 v37, 0x42000000, v53
	v_med3_f32 v36, v36, s83, v238
	v_med3_f32 v37, v37, s83, v238
	v_cvt_pk_fp8_f32 v35, v36, v37 op_sel:[0,0,1]
	v_lshl_add_u64 v[32:33], s[8:9], 0, v[6:7]
	v_lshl_add_u64 v[36:37], v[32:33], 0, v[10:11]
	ds_read2_b32 v[44:45], v50 offset0:148 offset1:156
	global_store_dwordx2 v[36:37], v[34:35], off nt
	ds_read2_b32 v[34:35], v50 offset0:16 offset1:24
	ds_read2_b32 v[36:37], v50 offset0:49 offset1:57
	ds_read2_b32 v[46:47], v50 offset0:181 offset1:189
	ds_read2_b32 v[38:39], v50 offset0:82 offset1:90
	ds_read2_b32 v[40:41], v50 offset0:115 offset1:123
	v_lshl_add_u64 v[54:55], v[32:33], 0, v[8:9]
	s_waitcnt lgkmcnt(4)
	v_mul_f32_e32 v3, 0x42000000, v34
	s_waitcnt lgkmcnt(3)
	v_mul_f32_e32 v34, 0x42000000, v36
	global_store_dwordx2 v[54:55], v[42:43], off nt
	v_med3_f32 v3, v3, s83, v238
	v_med3_f32 v34, v34, s83, v238
	v_mov_b32_e32 v42, v0
	ds_read2_b32 v[48:49], v50 offset0:214 offset1:222
	ds_read2_b32 v[52:53], v50 offset0:247 offset1:255
	v_cvt_pk_fp8_f32 v42, v3, v34
	v_mul_f32_e32 v3, 0x42000000, v44
	s_waitcnt lgkmcnt(4)
	v_mul_f32_e32 v34, 0x42000000, v46
	v_med3_f32 v3, v3, s83, v238
	v_med3_f32 v34, v34, s83, v238
	v_mov_b32_e32 v43, v0
	s_waitcnt lgkmcnt(3)
	v_mul_f32_e32 v36, 0x42000000, v38
	s_waitcnt lgkmcnt(2)
	v_mul_f32_e32 v38, 0x42000000, v40
	v_cvt_pk_fp8_f32 v43, v3, v34
	v_mul_f32_e32 v3, 0x42000000, v35
	v_mul_f32_e32 v34, 0x42000000, v37
	v_med3_f32 v36, v36, s83, v238
	v_med3_f32 v38, v38, s83, v238
	v_med3_f32 v3, v3, s83, v238
	v_med3_f32 v37, v34, s83, v238
	v_mov_b32_e32 v34, v0
	v_cvt_pk_fp8_f32 v42, v36, v38 op_sel:[0,0,1]
	s_waitcnt lgkmcnt(1)
	v_mul_f32_e32 v36, 0x42000000, v48
	s_waitcnt lgkmcnt(0)
	v_mul_f32_e32 v38, 0x42000000, v52
	v_cvt_pk_fp8_f32 v34, v3, v37
	v_med3_f32 v36, v36, s83, v238
	v_med3_f32 v38, v38, s83, v238
	v_cvt_pk_fp8_f32 v43, v36, v38 op_sel:[0,0,1]
	v_mul_f32_e32 v35, 0x42000000, v39
	v_mul_f32_e32 v36, 0x42000000, v41
	v_med3_f32 v35, v35, s83, v238
	v_med3_f32 v36, v36, s83, v238
	v_cvt_pk_fp8_f32 v34, v35, v36 op_sel:[0,0,1]
	v_mul_f32_e32 v3, 0x42000000, v45
	v_mul_f32_e32 v35, 0x42000000, v47
	v_med3_f32 v3, v3, s83, v238
	v_med3_f32 v38, v35, s83, v238
	v_mov_b32_e32 v35, v0
	v_cvt_pk_fp8_f32 v35, v3, v38
	v_mul_f32_e32 v36, 0x42000000, v49
	v_mul_f32_e32 v37, 0x42000000, v53
	v_med3_f32 v36, v36, s83, v238
	v_med3_f32 v37, v37, s83, v238
	v_cvt_pk_fp8_f32 v35, v36, v37 op_sel:[0,0,1]
	v_lshl_add_u64 v[54:55], v[32:33], 0, v[12:13]
	v_lshl_add_u64 v[32:33], v[32:33], 0, v[14:15]
	global_store_dwordx2 v[54:55], v[42:43], off nt
	global_store_dwordx2 v[32:33], v[34:35], off nt
	s_waitcnt lgkmcnt(0)
	s_add_u32 s8, s8, 0x8000
	s_addc_u32 s9, s9, 0
	s_add_u32 s18, s18, 0x200
	s_addc_u32 s19, s19, 0
	s_add_i32 s43, s43, 4
	s_cmp_lt_u32 s43, 16
	s_cbranch_scc1 .Lcv_dn_loop
	s_mov_b32 s43, 15
	s_branch .LBB0_819

; #define LAS __attribute__((address_space(3)))
; __device__ __forceinline__ void p0_transpose_item8(const float* W, int ldw, int srccol0, int k0, unsigned char* dst, int K, LAS float* scr, int lane) {
;     ...
;     const int c = lane & 7;
; #pragma unroll
;     for (int j = 0; j < 4; ++j) { const int n = (lane >> 3) + 8 * j; const LAS float* s = scr + (8 * c) * 33 + n;
;         u32x2 o; o.x = pk4_f8(s[0 * 33] * 32.f, s[1 * 33] * 32.f, s[2 * 33] * 32.f, s[3 * 33] * 32.f); o.y = pk4_f8(s[4 * 33] * 32.f, s[5 * 33] * 32.f, s[6 * 33] * 32.f, s[7 * 33] * 32.f);
;         *(u32x2*)(dst + (size_t)n * K + k0 + 8 * c) = o; }
.Lcv_gu_0_n:
	ds_read2_b32 v[34:35], v50 offset1:8
	ds_read2_b32 v[36:37], v50 offset0:33 offset1:41
	ds_read2_b32 v[44:45], v50 offset0:132 offset1:140
	ds_read2_b32 v[46:47], v50 offset0:165 offset1:173
	ds_read2_b32 v[38:39], v50 offset0:66 offset1:74
	ds_read2_b32 v[40:41], v50 offset0:99 offset1:107
	s_waitcnt lgkmcnt(5)
	v_mul_f32_e32 v3, 0x42000000, v34
	s_waitcnt lgkmcnt(4)
	v_mul_f32_e32 v34, 0x42000000, v36
	v_med3_f32 v3, v3, s83, v238
	v_med3_f32 v34, v34, s83, v238
	ds_read2_b32 v[48:49], v50 offset0:198 offset1:206
	ds_read2_b32 v[52:53], v50 offset0:231 offset1:239
	v_cvt_pk_fp8_f32 v42, v3, v34
	s_waitcnt lgkmcnt(5)
	v_mul_f32_e32 v3, 0x42000000, v44
	s_waitcnt lgkmcnt(4)
	v_mul_f32_e32 v34, 0x42000000, v46
	v_med3_f32 v3, v3, s83, v238
	v_med3_f32 v34, v34, s83, v238
	s_waitcnt lgkmcnt(3)
	v_mul_f32_e32 v36, 0x42000000, v38
	s_waitcnt lgkmcnt(2)
	v_mul_f32_e32 v38, 0x42000000, v40
	v_cvt_pk_fp8_f32 v43, v3, v34
	v_mul_f32_e32 v3, 0x42000000, v35
	v_mul_f32_e32 v34, 0x42000000, v37
	v_med3_f32 v36, v36, s83, v238
	v_med3_f32 v38, v38, s83, v238
	v_med3_f32 v3, v3, s83, v238
	v_med3_f32 v37, v34, s83, v238
	v_mov_b32_e32 v34, v0
	v_cvt_pk_fp8_f32 v42, v36, v38 op_sel:[0,0,1]
	s_waitcnt lgkmcnt(1)
	v_mul_f32_e32 v36, 0x42000000, v48
	s_waitcnt lgkmcnt(0)
	v_mul_f32_e32 v38, 0x42000000, v52
	v_cvt_pk_fp8_f32 v34, v3, v37
	v_med3_f32 v36, v36, s83, v238
	v_med3_f32 v38, v38, s83, v238
	v_cvt_pk_fp8_f32 v43, v36, v38 op_sel:[0,0,1]
	v_mul_f32_e32 v35, 0x42000000, v39
	v_mul_f32_e32 v36, 0x42000000, v41
	v_med3_f32 v35, v35, s83, v238
	v_med3_f32 v36, v36, s83, v238
	v_cvt_pk_fp8_f32 v34, v35, v36 op_sel:[0,0,1]
	v_mul_f32_e32 v3, 0x42000000, v45
	v_mul_f32_e32 v35, 0x42000000, v47
	v_med3_f32 v3, v3, s83, v238
	v_med3_f32 v38, v35, s83, v238
	v_mov_b32_e32 v35, v0
	v_cvt_pk_fp8_f32 v35, v3, v38
	v_mul_f32_e32 v36, 0x42000000, v49
	v_mul_f32_e32 v37, 0x42000000, v53
	v_med3_f32 v36, v36, s83, v238
	v_med3_f32 v37, v37, s83, v238
	v_cvt_pk_fp8_f32 v35, v36, v37 op_sel:[0,0,1]
	v_lshl_add_u64 v[32:33], s[8:9], 0, v[6:7]
	v_lshl_add_u64 v[36:37], v[32:33], 0, v[18:19]
	ds_read2_b32 v[44:45], v50 offset0:148 offset1:156
	global_store_dwordx2 v[36:37], v[34:35], off nt
	ds_read2_b32 v[34:35], v50 offset0:16 offset1:24
	ds_read2_b32 v[36:37], v50 offset0:49 offset1:57
	ds_read2_b32 v[46:47], v50 offset0:181 offset1:189
	ds_read2_b32 v[38:39], v50 offset0:82 offset1:90
	ds_read2_b32 v[40:41], v50 offset0:115 offset1:123
	v_lshl_add_u64 v[54:55], v[32:33], 0, v[16:17]
	s_waitcnt lgkmcnt(4)
	v_mul_f32_e32 v3, 0x42000000, v34
	s_waitcnt lgkmcnt(3)
	v_mul_f32_e32 v34, 0x42000000, v36
	global_store_dwordx2 v[54:55], v[42:43], off nt
	v_med3_f32 v3, v3, s83, v238
	v_med3_f32 v34, v34, s83, v238
	v_mov_b32_e32 v42, v0
	ds_read2_b32 v[48:49], v50 offset0:214 offset1:222
	ds_read2_b32 v[52:53], v50 offset0:247 offset1:255
	v_cvt_pk_fp8_f32 v42, v3, v34
	v_mul_f32_e32 v3, 0x42000000, v44
	s_waitcnt lgkmcnt(4)
	v_mul_f32_e32 v34, 0x42000000, v46
	v_med3_f32 v3, v3, s83, v238
	v_med3_f32 v34, v34, s83, v238
	v_mov_b32_e32 v43, v0
	s_waitcnt lgkmcnt(3)
	v_mul_f32_e32 v36, 0x42000000, v38
	s_waitcnt lgkmcnt(2)
	v_mul_f32_e32 v38, 0x42000000, v40
	v_cvt_pk_fp8_f32 v43, v3, v34
	v_mul_f32_e32 v3, 0x42000000, v35
	v_mul_f32_e32 v34, 0x42000000, v37
	v_med3_f32 v36, v36, s83, v238
	v_med3_f32 v38, v38, s83, v238
	v_med3_f32 v3, v3, s83, v238
	v_med3_f32 v37, v34, s83, v238
	v_mov_b32_e32 v34, v0
	v_cvt_pk_fp8_f32 v42, v36, v38 op_sel:[0,0,1]
	s_waitcnt lgkmcnt(1)
	v_mul_f32_e32 v36, 0x42000000, v48
	s_waitcnt lgkmcnt(0)
	v_mul_f32_e32 v38, 0x42000000, v52
	v_cvt_pk_fp8_f32 v34, v3, v37
	v_med3_f32 v36, v36, s83, v238
	v_med3_f32 v38, v38, s83, v238
	v_cvt_pk_fp8_f32 v43, v36, v38 op_sel:[0,0,1]
	v_mul_f32_e32 v35, 0x42000000, v39
	v_mul_f32_e32 v36, 0x42000000, v41
	v_med3_f32 v35, v35, s83, v238
	v_med3_f32 v36, v36, s83, v238
	v_cvt_pk_fp8_f32 v34, v35, v36 op_sel:[0,0,1]
	v_mul_f32_e32 v3, 0x42000000, v45
	v_mul_f32_e32 v35, 0x42000000, v47
	v_med3_f32 v3, v3, s83, v238
	v_med3_f32 v38, v35, s83, v238
	v_mov_b32_e32 v35, v0
	v_cvt_pk_fp8_f32 v35, v3, v38
	v_mul_f32_e32 v36, 0x42000000, v49
	v_mul_f32_e32 v37, 0x42000000, v53
	v_med3_f32 v36, v36, s83, v238
	v_med3_f32 v37, v37, s83, v238
	v_cvt_pk_fp8_f32 v35, v36, v37 op_sel:[0,0,1]
	v_lshl_add_u64 v[54:55], v[32:33], 0, v[20:21]
	v_lshl_add_u64 v[32:33], v[32:33], 0, v[22:23]
	global_store_dwordx2 v[54:55], v[42:43], off nt
	global_store_dwordx2 v[32:33], v[34:35], off nt
	s_waitcnt lgkmcnt(0)
	s_add_u32 s8, s8, 0x10000
	s_addc_u32 s9, s9, 0
	s_cmp_eq_u32 s43, 0
	s_cbranch_scc1 .Lcv_gu_1_f
	s_cmp_eq_u32 s43, 12
	s_cbranch_scc1 .Lcv_gu_1_l
	s_waitcnt vmcnt(40)
	s_branch .Lcv_gu_1_d

; #define LAS __attribute__((address_space(3)))
; __device__ __forceinline__ void p0_transpose_item8(const float* W, int ldw, int srccol0, int k0, unsigned char* dst, int K, LAS float* scr, int lane) {
;     ...
;     const int c = lane & 7;
; #pragma unroll
;     for (int j = 0; j < 4; ++j) { const int n = (lane >> 3) + 8 * j; const LAS float* s = scr + (8 * c) * 33 + n;
;         u32x2 o; o.x = pk4_f8(s[0 * 33] * 32.f, s[1 * 33] * 32.f, s[2 * 33] * 32.f, s[3 * 33] * 32.f); o.y = pk4_f8(s[4 * 33] * 32.f, s[5 * 33] * 32.f, s[6 * 33] * 32.f, s[7 * 33] * 32.f);
;         *(u32x2*)(dst + (size_t)n * K + k0 + 8 * c) = o; }
.Lcv_gu_3_n:
	ds_read2_b32 v[34:35], v50 offset1:8
	ds_read2_b32 v[36:37], v50 offset0:33 offset1:41
	ds_read2_b32 v[44:45], v50 offset0:132 offset1:140
	ds_read2_b32 v[46:47], v50 offset0:165 offset1:173
	ds_read2_b32 v[38:39], v50 offset0:66 offset1:74
	ds_read2_b32 v[40:41], v50 offset0:99 offset1:107
	s_waitcnt lgkmcnt(5)
	v_mul_f32_e32 v3, 0x42000000, v34
	s_waitcnt lgkmcnt(4)
	v_mul_f32_e32 v34, 0x42000000, v36
	v_med3_f32 v3, v3, s83, v238
	v_med3_f32 v34, v34, s83, v238
	ds_read2_b32 v[48:49], v50 offset0:198 offset1:206
	ds_read2_b32 v[52:53], v50 offset0:231 offset1:239
	v_cvt_pk_fp8_f32 v42, v3, v34
	s_waitcnt lgkmcnt(5)
	v_mul_f32_e32 v3, 0x42000000, v44
	s_waitcnt lgkmcnt(4)
	v_mul_f32_e32 v34, 0x42000000, v46
	v_med3_f32 v3, v3, s83, v238
	v_med3_f32 v34, v34, s83, v238
	s_waitcnt lgkmcnt(3)
	v_mul_f32_e32 v36, 0x42000000, v38
	s_waitcnt lgkmcnt(2)
	v_mul_f32_e32 v38, 0x42000000, v40
	v_cvt_pk_fp8_f32 v43, v3, v34
	v_mul_f32_e32 v3, 0x42000000, v35
	v_mul_f32_e32 v34, 0x42000000, v37
	v_med3_f32 v36, v36, s83, v238
	v_med3_f32 v38, v38, s83, v238
	v_med3_f32 v3, v3, s83, v238
	v_med3_f32 v37, v34, s83, v238
	v_mov_b32_e32 v34, v0
	v_cvt_pk_fp8_f32 v42, v36, v38 op_sel:[0,0,1]
	s_waitcnt lgkmcnt(1)
	v_mul_f32_e32 v36, 0x42000000, v48
	s_waitcnt lgkmcnt(0)
	v_mul_f32_e32 v38, 0x42000000, v52
	v_cvt_pk_fp8_f32 v34, v3, v37
	v_med3_f32 v36, v36, s83, v238
	v_med3_f32 v38, v38, s83, v238
	v_cvt_pk_fp8_f32 v43, v36, v38 op_sel:[0,0,1]
	v_mul_f32_e32 v35, 0x42000000, v39
	v_mul_f32_e32 v36, 0x42000000, v41
	v_med3_f32 v35, v35, s83, v238
	v_med3_f32 v36, v36, s83, v238
	v_cvt_pk_fp8_f32 v34, v35, v36 op_sel:[0,0,1]
	v_mul_f32_e32 v3, 0x42000000, v45
	v_mul_f32_e32 v35, 0x42000000, v47
	v_med3_f32 v3, v3, s83, v238
	v_med3_f32 v38, v35, s83, v238
	v_mov_b32_e32 v35, v0
	v_cvt_pk_fp8_f32 v35, v3, v38
	v_mul_f32_e32 v36, 0x42000000, v49
	v_mul_f32_e32 v37, 0x42000000, v53
	v_med3_f32 v36, v36, s83, v238
	v_med3_f32 v37, v37, s83, v238
	v_cvt_pk_fp8_f32 v35, v36, v37 op_sel:[0,0,1]
	v_lshl_add_u64 v[32:33], s[8:9], 0, v[6:7]
	v_lshl_add_u64 v[36:37], v[32:33], 0, v[18:19]
	ds_read2_b32 v[44:45], v50 offset0:148 offset1:156
	global_store_dwordx2 v[36:37], v[34:35], off nt
	ds_read2_b32 v[34:35], v50 offset0:16 offset1:24
	ds_read2_b32 v[36:37], v50 offset0:49 offset1:57
	ds_read2_b32 v[46:47], v50 offset0:181 offset1:189
	ds_read2_b32 v[38:39], v50 offset0:82 offset1:90
	ds_read2_b32 v[40:41], v50 offset0:115 offset1:123
	v_lshl_add_u64 v[54:55], v[32:33], 0, v[16:17]
	s_waitcnt lgkmcnt(4)
	v_mul_f32_e32 v3, 0x42000000, v34
	s_waitcnt lgkmcnt(3)
	v_mul_f32_e32 v34, 0x42000000, v36
	global_store_dwordx2 v[54:55], v[42:43], off nt
	v_med3_f32 v3, v3, s83, v238
	v_med3_f32 v34, v34, s83, v238
	v_mov_b32_e32 v42, v0
	ds_read2_b32 v[48:49], v50 offset0:214 offset1:222
	ds_read2_b32 v[52:53], v50 offset0:247 offset1:255
	v_cvt_pk_fp8_f32 v42, v3, v34
	v_mul_f32_e32 v3, 0x42000000, v44
	s_waitcnt lgkmcnt(4)
	v_mul_f32_e32 v34, 0x42000000, v46
	v_med3_f32 v3, v3, s83, v238
	v_med3_f32 v34, v34, s83, v238
	v_mov_b32_e32 v43, v0
	s_waitcnt lgkmcnt(3)
	v_mul_f32_e32 v36, 0x42000000, v38
	s_waitcnt lgkmcnt(2)
	v_mul_f32_e32 v38, 0x42000000, v40
	v_cvt_pk_fp8_f32 v43, v3, v34
	v_mul_f32_e32 v3, 0x42000000, v35
	v_mul_f32_e32 v34, 0x42000000, v37
	v_med3_f32 v36, v36, s83, v238
	v_med3_f32 v38, v38, s83, v238
	v_med3_f32 v3, v3, s83, v238
	v_med3_f32 v37, v34, s83, v238
	v_mov_b32_e32 v34, v0
	v_cvt_pk_fp8_f32 v42, v36, v38 op_sel:[0,0,1]
	s_waitcnt lgkmcnt(1)
	v_mul_f32_e32 v36, 0x42000000, v48
	s_waitcnt lgkmcnt(0)
	v_mul_f32_e32 v38, 0x42000000, v52
	v_cvt_pk_fp8_f32 v34, v3, v37
	v_med3_f32 v36, v36, s83, v238
	v_med3_f32 v38, v38, s83, v238
	v_cvt_pk_fp8_f32 v43, v36, v38 op_sel:[0,0,1]
	v_mul_f32_e32 v35, 0x42000000, v39
	v_mul_f32_e32 v36, 0x42000000, v41
	v_med3_f32 v35, v35, s83, v238
	v_med3_f32 v36, v36, s83, v238
	v_cvt_pk_fp8_f32 v34, v35, v36 op_sel:[0,0,1]
	v_mul_f32_e32 v3, 0x42000000, v45
	v_mul_f32_e32 v35, 0x42000000, v47
	v_med3_f32 v3, v3, s83, v238
	v_med3_f32 v38, v35, s83, v238
	v_mov_b32_e32 v35, v0
	v_cvt_pk_fp8_f32 v35, v3, v38
	v_mul_f32_e32 v36, 0x42000000, v49
	v_mul_f32_e32 v37, 0x42000000, v53
	v_med3_f32 v36, v36, s83, v238
	v_med3_f32 v37, v37, s83, v238
	v_cvt_pk_fp8_f32 v35, v36, v37 op_sel:[0,0,1]
	v_lshl_add_u64 v[54:55], v[32:33], 0, v[20:21]
	v_lshl_add_u64 v[32:33], v[32:33], 0, v[22:23]
	global_store_dwordx2 v[54:55], v[42:43], off nt
	global_store_dwordx2 v[32:33], v[34:35], off nt
	s_waitcnt lgkmcnt(0)
	s_add_u32 s8, s8, 0x10000
	s_addc_u32 s9, s9, 0
	s_mov_b32 s4, s18
	s_mov_b32 s5, s19
	s_mov_b32 s18, s26
	s_mov_b32 s19, s27
	s_add_u32 s26, s4, 0x200
	s_addc_u32 s27, s5, 0
	s_add_i32 s43, s43, 4
	s_cmp_lt_u32 s43, 16
	s_cbranch_scc1 .Lcv_gu_loop
	s_mov_b32 s43, 15
	s_branch .LBB0_819

; #define LAS __attribute__((address_space(3)))
; #define LDS_WAIT() asm volatile("s_waitcnt lgkmcnt(0)" ::: "memory")
; __device__ __forceinline__ void p0_transpose_item8(const float* W, int ldw, int srccol0, int k0, unsigned char* dst, int K, LAS float* scr, int lane) {
;     { f32x4 v[8];
; #pragma unroll
;       for (int i = 0; i < 8; ++i) v[i] = *(const f32x4*)(W + (size_t)(k0 + 8 * i + (lane >> 3)) * ldw + srccol0 + 4 * (lane & 7));
; #pragma unroll
;       for (int i = 0; i < 8; ++i) { LAS float* p = scr + (8 * i + (lane >> 3)) * 33 + 4 * (lane & 7); p[0] = v[i][0]; p[1] = v[i][1]; p[2] = v[i][2]; p[3] = v[i][3]; } }
;     LDS_WAIT(); asm volatile("" ::: "memory");
;     const int c = lane & 7;
; #pragma unroll
;     for (int j = 0; j < 4; ++j) { const int n = (lane >> 3) + 8 * j; const LAS float* s = scr + (8 * c) * 33 + n;
;         u32x2 o; o.x = pk4_f8(s[0 * 33] * 32.f, s[1 * 33] * 32.f, s[2 * 33] * 32.f, s[3 * 33] * 32.f); o.y = pk4_f8(s[4 * 33] * 32.f, s[5 * 33] * 32.f, s[6 * 33] * 32.f, s[7 * 33] * 32.f);
;         *(u32x2*)(dst + (size_t)n * K + k0 + 8 * c) = o; }
; __device__ __forceinline__ void p0_item(KP Pk, Frame& F, int it, LAS float* scr) {
;     ...
;     { const int le = it / TI_DN, r = it % TI_DN, kb = r / 64, nb = r % 64;
;         p0_transpose_item8(Pk->in[I_ED] + (size_t)le * DE * D, D, 32 * nb, 64 * kb, ws + WS_WD + ((size_t)le * D + 32 * nb) * DE, DE, scr, F.lane); }
.LBB0_836:
	s_cmp_gt_u32 s4, 0x13a3f
	s_cbranch_scc0 .LBB0_838
	s_cmp_eq_u32 s43, 0
	s_cbranch_scc1 .Lcv_dn
	s_load_dwordx2 s[8:9], s[48:49], 0x108
	s_add_i32 s5, s4, 0xfffec5c0
	s_lshr_b32 s60, s5, 10
	s_and_b32 s5, s5, 0x3c0
	s_lshl_b64 s[18:19], s[60:61], 23
	s_waitcnt lgkmcnt(0)
	s_add_u32 s18, s8, s18
	s_addc_u32 s19, s9, s19
	s_lshl_b32 s8, s4, 5
	s_and_b32 s26, s8, 0x7e0
	s_lshl_b64 s[8:9], s[60:61], 21
	s_lshl_b32 s27, s26, 10
	v_readlane_b32 s34, v255, 7
	s_add_u32 s8, s34, s8
	v_readlane_b32 s34, v255, 8
	s_addc_u32 s9, s34, s9
	s_add_u32 s27, s8, s27
	s_addc_u32 s34, s9, 0
	s_lshl_b32 s8, s26, 2
	v_add_u32_e32 v32, s5, v2
	s_add_u32 s8, s18, s8
	s_addc_u32 s9, s19, 0
	v_lshlrev_b32_e32 v34, 2, v4
	v_mov_b32_e32 v35, v0
	v_ashrrev_i32_e32 v33, 31, v32
	v_lshl_add_u64 v[34:35], s[8:9], 0, v[34:35]
	v_lshlrev_b64 v[32:33], 13, v[32:33]
	v_lshl_add_u64 v[48:49], v[34:35], 0, v[32:33]
	s_mov_b32 s8, 0x10000
	v_add_co_u32_e32 v36, vcc, s8, v48
	global_load_dwordx4 v[32:35], v[48:49], off nt
	s_nop 0
	v_addc_co_u32_e32 v37, vcc, 0, v49, vcc
	s_mov_b32 s8, 0x20000
	global_load_dwordx4 v[36:39], v[36:37], off nt
	v_add_co_u32_e32 v40, vcc, s8, v48
	s_mov_b32 s8, 0x30000
	s_nop 0
	v_addc_co_u32_e32 v41, vcc, 0, v49, vcc
	global_load_dwordx4 v[40:43], v[40:41], off nt
	v_add_co_u32_e32 v44, vcc, s8, v48
	s_mov_b32 s8, 0x40000
	s_nop 0
	v_addc_co_u32_e32 v45, vcc, 0, v49, vcc
	global_load_dwordx4 v[44:47], v[44:45], off nt
	v_add_co_u32_e32 v52, vcc, s8, v48
	s_mov_b32 s8, 0x50000
	s_nop 0
	v_addc_co_u32_e32 v53, vcc, 0, v49, vcc
	global_load_dwordx4 v[52:55], v[52:53], off nt
	v_add_co_u32_e32 v56, vcc, s8, v48
	s_mov_b32 s8, 0x60000
	s_nop 0
	v_addc_co_u32_e32 v57, vcc, 0, v49, vcc
	global_load_dwordx4 v[56:59], v[56:57], off nt
	v_add_co_u32_e32 v60, vcc, s8, v48
	s_mov_b32 s8, 0x70000
	s_nop 0
	v_addc_co_u32_e32 v61, vcc, 0, v49, vcc
	global_load_dwordx4 v[60:63], v[60:61], off nt
	v_add_co_u32_e32 v48, vcc, s8, v48
	v_add_u32_e32 v3, v1, v5
	s_nop 0
	v_addc_co_u32_e32 v49, vcc, 0, v49, vcc
	global_load_dwordx4 v[64:67], v[48:49], off nt
	s_add_u32 s8, s27, s5
	s_addc_u32 s9, s34, 0
	s_waitcnt vmcnt(7)
	ds_write2_b32 v3, v32, v33 offset1:1
	ds_write2_b32 v3, v34, v35 offset0:2 offset1:3
	v_add_u32_e32 v32, 0x420, v3
	s_waitcnt vmcnt(6)
	ds_write2_b32 v32, v36, v37 offset1:1
	v_add_u32_e32 v32, 0x428, v3
	ds_write2_b32 v32, v38, v39 offset1:1
	v_add_u32_e32 v32, 0x840, v3
	s_waitcnt vmcnt(5)
	ds_write2_b32 v32, v40, v41 offset1:1
	v_add_u32_e32 v32, 0x848, v3
	ds_write2_b32 v32, v42, v43 offset1:1
	v_add_u32_e32 v32, 0xc60, v3
	v_mov_b32_e32 v42, v0
	v_mov_b32_e32 v43, v0
	s_waitcnt vmcnt(4)
	ds_write2_b32 v32, v44, v45 offset1:1
	v_add_u32_e32 v32, 0xc68, v3
	ds_write2_b32 v32, v46, v47 offset1:1
	v_add_u32_e32 v32, 0x1080, v3
	s_waitcnt vmcnt(3)
	ds_write2_b32 v32, v52, v53 offset1:1
	v_add_u32_e32 v32, 0x1088, v3
	ds_write2_b32 v32, v54, v55 offset1:1
	v_add_u32_e32 v32, 0x14a0, v3
	s_waitcnt vmcnt(2)
	ds_write2_b32 v32, v56, v57 offset1:1
	v_add_u32_e32 v32, 0x14a8, v3
	ds_write2_b32 v32, v58, v59 offset1:1
	v_add_u32_e32 v32, 0x18c0, v3
	s_waitcnt vmcnt(1)
	ds_write2_b32 v32, v60, v61 offset1:1
	v_add_u32_e32 v32, 0x18c8, v3
	ds_write2_b32 v32, v62, v63 offset1:1
	v_add_u32_e32 v32, 0x1ce0, v3
	v_add_u32_e32 v3, 0x1ce8, v3
	s_waitcnt vmcnt(0)
	ds_write2_b32 v32, v64, v65 offset1:1
	ds_write2_b32 v3, v66, v67 offset1:1
	s_waitcnt lgkmcnt(0)
	ds_read2_b32 v[34:35], v50 offset1:8
	ds_read2_b32 v[36:37], v50 offset0:33 offset1:41
	ds_read2_b32 v[44:45], v50 offset0:132 offset1:140
	ds_read2_b32 v[46:47], v50 offset0:165 offset1:173
	ds_read2_b32 v[38:39], v50 offset0:66 offset1:74
	ds_read2_b32 v[40:41], v50 offset0:99 offset1:107
	s_waitcnt lgkmcnt(5)
	v_mul_f32_e32 v3, 0x42000000, v34
	s_waitcnt lgkmcnt(4)
	v_mul_f32_e32 v34, 0x42000000, v36
	v_med3_f32 v3, v3, s83, v238
	v_med3_f32 v34, v34, s83, v238
	ds_read2_b32 v[48:49], v50 offset0:198 offset1:206
	ds_read2_b32 v[52:53], v50 offset0:231 offset1:239
	v_cvt_pk_fp8_f32 v42, v3, v34
	s_waitcnt lgkmcnt(5)
	v_mul_f32_e32 v3, 0x42000000, v44
	s_waitcnt lgkmcnt(4)
	v_mul_f32_e32 v34, 0x42000000, v46
	v_med3_f32 v3, v3, s83, v238
	v_med3_f32 v34, v34, s83, v238
	s_waitcnt lgkmcnt(3)
	v_mul_f32_e32 v36, 0x42000000, v38
	s_waitcnt lgkmcnt(2)
	v_mul_f32_e32 v38, 0x42000000, v40
	v_cvt_pk_fp8_f32 v43, v3, v34
	v_mul_f32_e32 v3, 0x42000000, v35
	v_mul_f32_e32 v34, 0x42000000, v37
	v_med3_f32 v36, v36, s83, v238
	v_med3_f32 v38, v38, s83, v238
	v_med3_f32 v3, v3, s83, v238
	v_med3_f32 v37, v34, s83, v238
	v_mov_b32_e32 v34, v0
	v_cvt_pk_fp8_f32 v42, v36, v38 op_sel:[0,0,1]
	s_waitcnt lgkmcnt(1)
	v_mul_f32_e32 v36, 0x42000000, v48
	s_waitcnt lgkmcnt(0)
	v_mul_f32_e32 v38, 0x42000000, v52
	v_cvt_pk_fp8_f32 v34, v3, v37
	v_med3_f32 v36, v36, s83, v238
	v_med3_f32 v38, v38, s83, v238
	v_cvt_pk_fp8_f32 v43, v36, v38 op_sel:[0,0,1]
	v_mul_f32_e32 v35, 0x42000000, v39
	v_mul_f32_e32 v36, 0x42000000, v41
	v_med3_f32 v35, v35, s83, v238
	v_med3_f32 v36, v36, s83, v238
	v_cvt_pk_fp8_f32 v34, v35, v36 op_sel:[0,0,1]
	v_mul_f32_e32 v3, 0x42000000, v45
	v_mul_f32_e32 v35, 0x42000000, v47
	v_med3_f32 v3, v3, s83, v238
	v_med3_f32 v38, v35, s83, v238
	v_mov_b32_e32 v35, v0
	v_cvt_pk_fp8_f32 v35, v3, v38
	v_mul_f32_e32 v36, 0x42000000, v49
	v_mul_f32_e32 v37, 0x42000000, v53
	v_med3_f32 v36, v36, s83, v238
	v_med3_f32 v37, v37, s83, v238
	v_cvt_pk_fp8_f32 v35, v36, v37 op_sel:[0,0,1]
	v_lshl_add_u64 v[32:33], s[8:9], 0, v[6:7]
	v_lshl_add_u64 v[36:37], v[32:33], 0, v[10:11]
	ds_read2_b32 v[44:45], v50 offset0:148 offset1:156
	global_store_dwordx2 v[36:37], v[34:35], off nt
	ds_read2_b32 v[34:35], v50 offset0:16 offset1:24
	ds_read2_b32 v[36:37], v50 offset0:49 offset1:57
	ds_read2_b32 v[46:47], v50 offset0:181 offset1:189
	ds_read2_b32 v[38:39], v50 offset0:82 offset1:90
	ds_read2_b32 v[40:41], v50 offset0:115 offset1:123
	v_lshl_add_u64 v[54:55], v[32:33], 0, v[8:9]
	s_waitcnt lgkmcnt(4)
; #define LAS __attribute__((address_space(3)))
; __device__ __forceinline__ void p0_transpose_item8(const float* W, int ldw, int srccol0, int k0, unsigned char* dst, int K, LAS float* scr, int lane) {
;     ...
;     const int c = lane & 7;
; #pragma unroll
;     for (int j = 0; j < 4; ++j) { const int n = (lane >> 3) + 8 * j; const LAS float* s = scr + (8 * c) * 33 + n;
;         u32x2 o; o.x = pk4_f8(s[0 * 33] * 32.f, s[1 * 33] * 32.f, s[2 * 33] * 32.f, s[3 * 33] * 32.f); o.y = pk4_f8(s[4 * 33] * 32.f, s[5 * 33] * 32.f, s[6 * 33] * 32.f, s[7 * 33] * 32.f);
;         *(u32x2*)(dst + (size_t)n * K + k0 + 8 * c) = o; }
; __device__ __forceinline__ void p0_item(KP Pk, Frame& F, int it, LAS float* scr) {
;     ...
;     if (it < 32 * TI_GU) { const int le = it / TI_GU, r = it % TI_GU, kb = r / 64, nb = r % 64, n0 = 32 * nb, j = n0 >> 8, half = (n0 >> 7) & 1, c0 = 128 * j + (n0 & 127);
;         p0_transpose_item8((half ? Pk->in[I_EU] : Pk->in[I_EG]) + (size_t)le * D * DE, DE, c0, 64 * kb, ws + WS_WGU + ((size_t)le * 2048 + n0) * D, D, scr, F.lane); return; }
	v_mul_f32_e32 v3, 0x42000000, v34
	s_waitcnt lgkmcnt(3)
	v_mul_f32_e32 v34, 0x42000000, v36
	global_store_dwordx2 v[54:55], v[42:43], off nt
	v_med3_f32 v3, v3, s83, v238
	v_med3_f32 v34, v34, s83, v238
	v_mov_b32_e32 v42, v0
	ds_read2_b32 v[48:49], v50 offset0:214 offset1:222
	ds_read2_b32 v[52:53], v50 offset0:247 offset1:255
	v_cvt_pk_fp8_f32 v42, v3, v34
	v_mul_f32_e32 v3, 0x42000000, v44
	s_waitcnt lgkmcnt(4)
	v_mul_f32_e32 v34, 0x42000000, v46
	v_med3_f32 v3, v3, s83, v238
	v_med3_f32 v34, v34, s83, v238
	v_mov_b32_e32 v43, v0
	s_waitcnt lgkmcnt(3)
	v_mul_f32_e32 v36, 0x42000000, v38
	s_waitcnt lgkmcnt(2)
	v_mul_f32_e32 v38, 0x42000000, v40
	v_cvt_pk_fp8_f32 v43, v3, v34
	v_mul_f32_e32 v3, 0x42000000, v35
	v_mul_f32_e32 v34, 0x42000000, v37
	v_med3_f32 v36, v36, s83, v238
	v_med3_f32 v38, v38, s83, v238
	v_med3_f32 v3, v3, s83, v238
	v_med3_f32 v37, v34, s83, v238
	v_mov_b32_e32 v34, v0
	v_cvt_pk_fp8_f32 v42, v36, v38 op_sel:[0,0,1]
	s_waitcnt lgkmcnt(1)
	v_mul_f32_e32 v36, 0x42000000, v48
	s_waitcnt lgkmcnt(0)
	v_mul_f32_e32 v38, 0x42000000, v52
	v_cvt_pk_fp8_f32 v34, v3, v37
	v_med3_f32 v36, v36, s83, v238
	v_med3_f32 v38, v38, s83, v238
	v_cvt_pk_fp8_f32 v43, v36, v38 op_sel:[0,0,1]
	v_mul_f32_e32 v35, 0x42000000, v39
	v_mul_f32_e32 v36, 0x42000000, v41
	v_med3_f32 v35, v35, s83, v238
	v_med3_f32 v36, v36, s83, v238
	v_cvt_pk_fp8_f32 v34, v35, v36 op_sel:[0,0,1]
	v_mul_f32_e32 v3, 0x42000000, v45
	v_mul_f32_e32 v35, 0x42000000, v47
	v_med3_f32 v3, v3, s83, v238
	v_med3_f32 v38, v35, s83, v238
	v_mov_b32_e32 v35, v0
	v_cvt_pk_fp8_f32 v35, v3, v38
	v_mul_f32_e32 v36, 0x42000000, v49
	v_mul_f32_e32 v37, 0x42000000, v53
	v_med3_f32 v36, v36, s83, v238
	v_med3_f32 v37, v37, s83, v238
	v_cvt_pk_fp8_f32 v35, v36, v37 op_sel:[0,0,1]
	v_lshl_add_u64 v[54:55], v[32:33], 0, v[12:13]
	v_lshl_add_u64 v[32:33], v[32:33], 0, v[14:15]
	global_store_dwordx2 v[54:55], v[42:43], off nt
	global_store_dwordx2 v[32:33], v[34:35], off nt
	s_waitcnt lgkmcnt(0)
	s_mov_b64 s[8:9], 0
.LBB0_838:
	s_andn2_b64 vcc, exec, s[8:9]
	s_cbranch_vccnz .LBB0_840
	s_cmp_eq_u32 s43, 0
	s_cbranch_scc1 .Lcv_gu
	s_lshl_b32 s8, s4, 5
	s_lshl_b32 s9, s4, 4
	s_add_i32 s5, s4, 0xffffc5c0
	s_waitcnt lgkmcnt(0)
	s_and_b32 s26, s8, 0x7e0
	s_and_b32 s9, s9, 0x380
	s_and_b32 s8, s8, 0x60
	s_and_b32 s60, s5, 0xfffff800
	s_and_b32 s5, s5, 0x7c0
	s_or_b32 s27, s9, s8
	s_bitcmp0_b32 s4, 2
	s_movk_i32 s8, 0xf8
	s_cselect_b32 s8, s8, 0x100
	s_add_u32 s8, s48, s8
	s_addc_u32 s9, s49, 0
	s_load_dwordx2 s[8:9], s[8:9], 0x0
	s_lshl_b64 s[18:19], s[60:61], 12
	v_add_u32_e32 v32, s5, v2
	v_lshlrev_b32_e32 v34, 2, v4
	v_mov_b32_e32 v35, v0
	s_waitcnt lgkmcnt(0)
	s_add_u32 s18, s8, s18
	s_addc_u32 s19, s9, s19
	s_or_b32 s60, s60, s26
	s_lshl_b64 s[8:9], s[60:61], 11
	v_readlane_b32 s26, v255, 9
	s_add_u32 s26, s26, s8
	v_readlane_b32 s8, v255, 10
	s_addc_u32 s34, s8, s9
	s_lshl_b32 s8, s27, 2
	s_add_u32 s8, s18, s8
	s_addc_u32 s9, s19, 0
	v_ashrrev_i32_e32 v33, 31, v32
	v_lshl_add_u64 v[34:35], s[8:9], 0, v[34:35]
	v_lshlrev_b64 v[32:33], 12, v[32:33]
	v_lshl_add_u64 v[48:49], v[34:35], 0, v[32:33]
	s_mov_b32 s8, 0x8000
	v_add_co_u32_e32 v36, vcc, s8, v48
	global_load_dwordx4 v[32:35], v[48:49], off nt
	s_nop 0
	v_addc_co_u32_e32 v37, vcc, 0, v49, vcc
	s_mov_b32 s8, 0x10000
	global_load_dwordx4 v[36:39], v[36:37], off nt
	v_add_co_u32_e32 v40, vcc, s8, v48
	s_mov_b32 s8, 0x18000
	s_nop 0
	v_addc_co_u32_e32 v41, vcc, 0, v49, vcc
	global_load_dwordx4 v[40:43], v[40:41], off nt
	v_add_co_u32_e32 v44, vcc, s8, v48
	s_mov_b32 s8, 0x20000
	s_nop 0
	v_addc_co_u32_e32 v45, vcc, 0, v49, vcc
	global_load_dwordx4 v[44:47], v[44:45], off nt
	v_add_co_u32_e32 v52, vcc, s8, v48
	s_mov_b32 s8, 0x28000
	s_nop 0
	v_addc_co_u32_e32 v53, vcc, 0, v49, vcc
	global_load_dwordx4 v[52:55], v[52:53], off nt
	v_add_co_u32_e32 v56, vcc, s8, v48
	s_mov_b32 s8, 0x30000
	s_nop 0
	v_addc_co_u32_e32 v57, vcc, 0, v49, vcc
	global_load_dwordx4 v[56:59], v[56:57], off nt
	v_add_co_u32_e32 v60, vcc, s8, v48
	s_mov_b32 s8, 0x38000
	s_nop 0
	v_addc_co_u32_e32 v61, vcc, 0, v49, vcc
	global_load_dwordx4 v[60:63], v[60:61], off nt
	v_add_co_u32_e32 v48, vcc, s8, v48
	v_add_u32_e32 v3, v1, v5
	s_nop 0
	v_addc_co_u32_e32 v49, vcc, 0, v49, vcc
	global_load_dwordx4 v[64:67], v[48:49], off nt
	s_add_u32 s8, s26, s5
	s_addc_u32 s9, s34, 0
	s_waitcnt vmcnt(7)
	ds_write2_b32 v3, v32, v33 offset1:1
	ds_write2_b32 v3, v34, v35 offset0:2 offset1:3
	v_add_u32_e32 v32, 0x420, v3
	s_waitcnt vmcnt(6)
	ds_write2_b32 v32, v36, v37 offset1:1
	v_add_u32_e32 v32, 0x428, v3
	ds_write2_b32 v32, v38, v39 offset1:1
	v_add_u32_e32 v32, 0x840, v3
	s_waitcnt vmcnt(5)
	ds_write2_b32 v32, v40, v41 offset1:1
	v_add_u32_e32 v32, 0x848, v3
	ds_write2_b32 v32, v42, v43 offset1:1
	v_add_u32_e32 v32, 0xc60, v3
	v_mov_b32_e32 v42, v0
	v_mov_b32_e32 v43, v0
	s_waitcnt vmcnt(4)
	ds_write2_b32 v32, v44, v45 offset1:1
	v_add_u32_e32 v32, 0xc68, v3
	ds_write2_b32 v32, v46, v47 offset1:1
	v_add_u32_e32 v32, 0x1080, v3
	s_waitcnt vmcnt(3)
; #define LAS __attribute__((address_space(3)))
; #define LDS_WAIT() asm volatile("s_waitcnt lgkmcnt(0)" ::: "memory")
; __device__ __forceinline__ void p0_transpose_item8(const float* W, int ldw, int srccol0, int k0, unsigned char* dst, int K, LAS float* scr, int lane) {
;     { f32x4 v[8];
; #pragma unroll
;       for (int i = 0; i < 8; ++i) v[i] = *(const f32x4*)(W + (size_t)(k0 + 8 * i + (lane >> 3)) * ldw + srccol0 + 4 * (lane & 7));
; #pragma unroll
;       for (int i = 0; i < 8; ++i) { LAS float* p = scr + (8 * i + (lane >> 3)) * 33 + 4 * (lane & 7); p[0] = v[i][0]; p[1] = v[i][1]; p[2] = v[i][2]; p[3] = v[i][3]; } }
;     LDS_WAIT(); asm volatile("" ::: "memory");
;     const int c = lane & 7;
; #pragma unroll
;     for (int j = 0; j < 4; ++j) { const int n = (lane >> 3) + 8 * j; const LAS float* s = scr + (8 * c) * 33 + n;
;         u32x2 o; o.x = pk4_f8(s[0 * 33] * 32.f, s[1 * 33] * 32.f, s[2 * 33] * 32.f, s[3 * 33] * 32.f); o.y = pk4_f8(s[4 * 33] * 32.f, s[5 * 33] * 32.f, s[6 * 33] * 32.f, s[7 * 33] * 32.f);
;         *(u32x2*)(dst + (size_t)n * K + k0 + 8 * c) = o; }
	ds_write2_b32 v32, v52, v53 offset1:1
	v_add_u32_e32 v32, 0x1088, v3
	ds_write2_b32 v32, v54, v55 offset1:1
	v_add_u32_e32 v32, 0x14a0, v3
	s_waitcnt vmcnt(2)
	ds_write2_b32 v32, v56, v57 offset1:1
	v_add_u32_e32 v32, 0x14a8, v3
	ds_write2_b32 v32, v58, v59 offset1:1
	v_add_u32_e32 v32, 0x18c0, v3
	s_waitcnt vmcnt(1)
	ds_write2_b32 v32, v60, v61 offset1:1
	v_add_u32_e32 v32, 0x18c8, v3
	ds_write2_b32 v32, v62, v63 offset1:1
	v_add_u32_e32 v32, 0x1ce0, v3
	v_add_u32_e32 v3, 0x1ce8, v3
	s_waitcnt vmcnt(0)
	ds_write2_b32 v32, v64, v65 offset1:1
	ds_write2_b32 v3, v66, v67 offset1:1
	s_waitcnt lgkmcnt(0)
	ds_read2_b32 v[34:35], v50 offset1:8
	ds_read2_b32 v[36:37], v50 offset0:33 offset1:41
	ds_read2_b32 v[44:45], v50 offset0:132 offset1:140
	ds_read2_b32 v[46:47], v50 offset0:165 offset1:173
	ds_read2_b32 v[38:39], v50 offset0:66 offset1:74
	ds_read2_b32 v[40:41], v50 offset0:99 offset1:107
	s_waitcnt lgkmcnt(5)
	v_mul_f32_e32 v3, 0x42000000, v34
	s_waitcnt lgkmcnt(4)
	v_mul_f32_e32 v34, 0x42000000, v36
	v_med3_f32 v3, v3, s83, v238
	v_med3_f32 v34, v34, s83, v238
	ds_read2_b32 v[48:49], v50 offset0:198 offset1:206
	ds_read2_b32 v[52:53], v50 offset0:231 offset1:239
	v_cvt_pk_fp8_f32 v42, v3, v34
	s_waitcnt lgkmcnt(5)
	v_mul_f32_e32 v3, 0x42000000, v44
	s_waitcnt lgkmcnt(4)
	v_mul_f32_e32 v34, 0x42000000, v46
	v_med3_f32 v3, v3, s83, v238
	v_med3_f32 v34, v34, s83, v238
	s_waitcnt lgkmcnt(3)
	v_mul_f32_e32 v36, 0x42000000, v38
	s_waitcnt lgkmcnt(2)
	v_mul_f32_e32 v38, 0x42000000, v40
	v_cvt_pk_fp8_f32 v43, v3, v34
	v_mul_f32_e32 v3, 0x42000000, v35
	v_mul_f32_e32 v34, 0x42000000, v37
	v_med3_f32 v36, v36, s83, v238
	v_med3_f32 v38, v38, s83, v238
	v_med3_f32 v3, v3, s83, v238
	v_med3_f32 v37, v34, s83, v238
	v_mov_b32_e32 v34, v0
	v_cvt_pk_fp8_f32 v42, v36, v38 op_sel:[0,0,1]
	s_waitcnt lgkmcnt(1)
	v_mul_f32_e32 v36, 0x42000000, v48
	s_waitcnt lgkmcnt(0)
	v_mul_f32_e32 v38, 0x42000000, v52
	v_cvt_pk_fp8_f32 v34, v3, v37
	v_med3_f32 v36, v36, s83, v238
	v_med3_f32 v38, v38, s83, v238
	v_cvt_pk_fp8_f32 v43, v36, v38 op_sel:[0,0,1]
	v_mul_f32_e32 v35, 0x42000000, v39
	v_mul_f32_e32 v36, 0x42000000, v41
	v_med3_f32 v35, v35, s83, v238
	v_med3_f32 v36, v36, s83, v238
	v_cvt_pk_fp8_f32 v34, v35, v36 op_sel:[0,0,1]
	v_mul_f32_e32 v3, 0x42000000, v45
	v_mul_f32_e32 v35, 0x42000000, v47
	v_med3_f32 v3, v3, s83, v238
	v_med3_f32 v38, v35, s83, v238
	v_mov_b32_e32 v35, v0
	v_cvt_pk_fp8_f32 v35, v3, v38
	v_mul_f32_e32 v36, 0x42000000, v49
	v_mul_f32_e32 v37, 0x42000000, v53
	v_med3_f32 v36, v36, s83, v238
	v_med3_f32 v37, v37, s83, v238
	v_cvt_pk_fp8_f32 v35, v36, v37 op_sel:[0,0,1]
	v_lshl_add_u64 v[32:33], s[8:9], 0, v[6:7]
	v_lshl_add_u64 v[36:37], v[32:33], 0, v[18:19]
	ds_read2_b32 v[44:45], v50 offset0:148 offset1:156
	global_store_dwordx2 v[36:37], v[34:35], off nt
	ds_read2_b32 v[34:35], v50 offset0:16 offset1:24
	ds_read2_b32 v[36:37], v50 offset0:49 offset1:57
	ds_read2_b32 v[46:47], v50 offset0:181 offset1:189
	ds_read2_b32 v[38:39], v50 offset0:82 offset1:90
	ds_read2_b32 v[40:41], v50 offset0:115 offset1:123
	v_lshl_add_u64 v[54:55], v[32:33], 0, v[16:17]
	s_waitcnt lgkmcnt(4)
	v_mul_f32_e32 v3, 0x42000000, v34
	s_waitcnt lgkmcnt(3)
	v_mul_f32_e32 v34, 0x42000000, v36
	global_store_dwordx2 v[54:55], v[42:43], off nt
	v_med3_f32 v3, v3, s83, v238
	v_med3_f32 v34, v34, s83, v238
	v_mov_b32_e32 v42, v0
	ds_read2_b32 v[48:49], v50 offset0:214 offset1:222
	ds_read2_b32 v[52:53], v50 offset0:247 offset1:255
	v_cvt_pk_fp8_f32 v42, v3, v34
	v_mul_f32_e32 v3, 0x42000000, v44
	s_waitcnt lgkmcnt(4)
	v_mul_f32_e32 v34, 0x42000000, v46
	v_med3_f32 v3, v3, s83, v238
	v_med3_f32 v34, v34, s83, v238
	v_mov_b32_e32 v43, v0
	s_waitcnt lgkmcnt(3)
	v_mul_f32_e32 v36, 0x42000000, v38
	s_waitcnt lgkmcnt(2)
	v_mul_f32_e32 v38, 0x42000000, v40
	v_cvt_pk_fp8_f32 v43, v3, v34
	v_mul_f32_e32 v3, 0x42000000, v35
	v_mul_f32_e32 v34, 0x42000000, v37
	v_med3_f32 v36, v36, s83, v238
	v_med3_f32 v38, v38, s83, v238
	v_med3_f32 v3, v3, s83, v238
	v_med3_f32 v37, v34, s83, v238
	v_mov_b32_e32 v34, v0
	v_cvt_pk_fp8_f32 v42, v36, v38 op_sel:[0,0,1]
	s_waitcnt lgkmcnt(1)
	v_mul_f32_e32 v36, 0x42000000, v48
	s_waitcnt lgkmcnt(0)
	v_mul_f32_e32 v38, 0x42000000, v52
	v_cvt_pk_fp8_f32 v34, v3, v37
	v_med3_f32 v36, v36, s83, v238
	v_med3_f32 v38, v38, s83, v238
	v_cvt_pk_fp8_f32 v43, v36, v38 op_sel:[0,0,1]
	v_mul_f32_e32 v35, 0x42000000, v39
	v_mul_f32_e32 v36, 0x42000000, v41
	v_med3_f32 v35, v35, s83, v238
	v_med3_f32 v36, v36, s83, v238
	v_cvt_pk_fp8_f32 v34, v35, v36 op_sel:[0,0,1]
	v_mul_f32_e32 v3, 0x42000000, v45
	v_mul_f32_e32 v35, 0x42000000, v47
	v_med3_f32 v3, v3, s83, v238
	v_med3_f32 v38, v35, s83, v238
	v_mov_b32_e32 v35, v0
	v_cvt_pk_fp8_f32 v35, v3, v38
	v_mul_f32_e32 v36, 0x42000000, v49
	v_mul_f32_e32 v37, 0x42000000, v53
	v_med3_f32 v36, v36, s83, v238
	v_med3_f32 v37, v37, s83, v238
	v_cvt_pk_fp8_f32 v35, v36, v37 op_sel:[0,0,1]
	v_lshl_add_u64 v[54:55], v[32:33], 0, v[20:21]
	v_lshl_add_u64 v[32:33], v[32:33], 0, v[22:23]
	global_store_dwordx2 v[54:55], v[42:43], off nt
	global_store_dwordx2 v[32:33], v[34:35], off nt
	s_waitcnt lgkmcnt(0)

; #define LAS __attribute__((address_space(3)))
; #define LDS_WAIT() asm volatile("s_waitcnt lgkmcnt(0)" ::: "memory")
; __device__ __forceinline__ void p0_transpose_item8(const float* W, int ldw, int srccol0, int k0, unsigned char* dst, int K, LAS float* scr, int lane) {
;     { f32x4 v[8];
; #pragma unroll
;       for (int i = 0; i < 8; ++i) v[i] = *(const f32x4*)(W + (size_t)(k0 + 8 * i + (lane >> 3)) * ldw + srccol0 + 4 * (lane & 7));
; #pragma unroll
;       for (int i = 0; i < 8; ++i) { LAS float* p = scr + (8 * i + (lane >> 3)) * 33 + 4 * (lane & 7); p[0] = v[i][0]; p[1] = v[i][1]; p[2] = v[i][2]; p[3] = v[i][3]; } }
;     LDS_WAIT(); asm volatile("" ::: "memory");
;     const int c = lane & 7;
; #pragma unroll
;     for (int j = 0; j < 4; ++j) { const int n = (lane >> 3) + 8 * j; const LAS float* s = scr + (8 * c) * 33 + n;
;         u32x2 o; o.x = pk4_f8(s[0 * 33] * 32.f, s[1 * 33] * 32.f, s[2 * 33] * 32.f, s[3 * 33] * 32.f); o.y = pk4_f8(s[4 * 33] * 32.f, s[5 * 33] * 32.f, s[6 * 33] * 32.f, s[7 * 33] * 32.f);
;         *(u32x2*)(dst + (size_t)n * K + k0 + 8 * c) = o; }
; __device__ __forceinline__ void p0_item(KP Pk, Frame& F, int it, LAS float* scr) {
;     ...
;         { const int kb = r / 64, nb = r % 64;
;           if (WOUT_F8) p0_transpose_item8(Pk->in[I_WOUT] + (size_t)l * D * D, D, 32 * nb, 64 * kb, ws + WS_WOUT + ((size_t)l * D + 32 * nb) * D, D, scr, F.lane);
;           else p0_transpose_item(Pk->in[I_WOUT] + (size_t)l * D * D, D, 32 * nb, 64 * kb, (bf16_t*)(ws + WS_WOUT) + ((size_t)l * D + 32 * nb) * D, D, scr, F.lane); return; }
.LBB0_841:
	s_mul_hi_i32 s5, s4, 0x8ca29c05
	s_add_i32 s5, s5, s4
	s_lshr_b32 s8, s5, 31
	s_ashr_i32 s5, s5, 12
	s_add_i32 s60, s5, s8
	s_mul_i32 s5, s60, 0x1d20
	s_sub_i32 s4, s4, s5
	s_cmpk_gt_i32 s4, 0x14ff
	s_mov_b64 s[8:9], -1
	s_cbranch_scc0 .LBB0_850
	s_cmpk_gt_u32 s4, 0x151f
	s_cbranch_scc0 .LBB0_844
	s_load_dwordx2 s[8:9], s[48:49], 0x48
	s_add_i32 s5, s4, 0xffffeae0
	s_ashr_i32 s19, s60, 31
	s_mov_b32 s18, s60
	s_and_b32 s34, s5, 0xffffffc0
	s_waitcnt lgkmcnt(0)
	s_lshl_b64 s[26:27], s[18:19], 24
	s_waitcnt lgkmcnt(0)
	s_add_u32 s26, s8, s26
	s_addc_u32 s27, s9, s27
	s_lshl_b32 s5, s5, 5
	s_and_b32 s5, s5, 0x7e0
	s_lshl_b64 s[8:9], s[18:19], 22
	s_lshl_b32 s18, s5, 11
	v_readlane_b32 s19, v255, 11
	s_add_u32 s8, s19, s8
	v_readlane_b32 s19, v255, 12
	s_addc_u32 s9, s19, s9
	s_add_u32 s18, s8, s18
	s_addc_u32 s19, s9, 0
	s_lshl_b32 s5, s5, 2
	v_add_u32_e32 v32, s34, v2
	s_add_u32 s8, s26, s5
	s_addc_u32 s9, s27, 0
	v_lshlrev_b32_e32 v34, 2, v4
	v_mov_b32_e32 v35, v0
	v_ashrrev_i32_e32 v33, 31, v32
	v_lshl_add_u64 v[34:35], s[8:9], 0, v[34:35]
	v_lshlrev_b64 v[32:33], 13, v[32:33]
	v_lshl_add_u64 v[48:49], v[34:35], 0, v[32:33]
	s_mov_b32 s5, 0x10000
	v_add_co_u32_e32 v36, vcc, s5, v48
	global_load_dwordx4 v[32:35], v[48:49], off nt
	s_nop 0
	v_addc_co_u32_e32 v37, vcc, 0, v49, vcc
	s_mov_b32 s5, 0x20000
	global_load_dwordx4 v[36:39], v[36:37], off nt
	v_add_co_u32_e32 v40, vcc, s5, v48
	s_mov_b32 s5, 0x30000
	s_nop 0
	v_addc_co_u32_e32 v41, vcc, 0, v49, vcc
	global_load_dwordx4 v[40:43], v[40:41], off nt
	v_add_co_u32_e32 v44, vcc, s5, v48
	s_mov_b32 s5, 0x40000
	s_nop 0
	v_addc_co_u32_e32 v45, vcc, 0, v49, vcc
	global_load_dwordx4 v[44:47], v[44:45], off nt
	v_add_co_u32_e32 v52, vcc, s5, v48
	s_mov_b32 s5, 0x50000
	s_nop 0
	v_addc_co_u32_e32 v53, vcc, 0, v49, vcc
	global_load_dwordx4 v[52:55], v[52:53], off nt
	v_add_co_u32_e32 v56, vcc, s5, v48
	s_mov_b32 s5, 0x60000
	s_nop 0
	v_addc_co_u32_e32 v57, vcc, 0, v49, vcc
	global_load_dwordx4 v[56:59], v[56:57], off nt
	v_add_co_u32_e32 v60, vcc, s5, v48
	s_mov_b32 s5, 0x70000
	s_nop 0
	v_addc_co_u32_e32 v61, vcc, 0, v49, vcc
	global_load_dwordx4 v[60:63], v[60:61], off nt
	v_add_co_u32_e32 v48, vcc, s5, v48
	v_add_u32_e32 v3, v1, v5
	s_nop 0
	v_addc_co_u32_e32 v49, vcc, 0, v49, vcc
	global_load_dwordx4 v[64:67], v[48:49], off nt
	s_add_u32 s8, s18, s34
	s_addc_u32 s9, s19, 0
	s_waitcnt vmcnt(7)
	ds_write2_b32 v3, v32, v33 offset1:1
	ds_write2_b32 v3, v34, v35 offset0:2 offset1:3
	v_add_u32_e32 v32, 0x420, v3
	s_waitcnt vmcnt(6)
	ds_write2_b32 v32, v36, v37 offset1:1
	v_add_u32_e32 v32, 0x428, v3
	ds_write2_b32 v32, v38, v39 offset1:1
	v_add_u32_e32 v32, 0x840, v3
	s_waitcnt vmcnt(5)
	ds_write2_b32 v32, v40, v41 offset1:1
	v_add_u32_e32 v32, 0x848, v3
	ds_write2_b32 v32, v42, v43 offset1:1
	v_add_u32_e32 v32, 0xc60, v3
	v_mov_b32_e32 v42, v0
	v_mov_b32_e32 v43, v0
	s_waitcnt vmcnt(4)
	ds_write2_b32 v32, v44, v45 offset1:1
	v_add_u32_e32 v32, 0xc68, v3
	ds_write2_b32 v32, v46, v47 offset1:1
	v_add_u32_e32 v32, 0x1080, v3
	s_waitcnt vmcnt(3)
	ds_write2_b32 v32, v52, v53 offset1:1
	v_add_u32_e32 v32, 0x1088, v3
	ds_write2_b32 v32, v54, v55 offset1:1
	v_add_u32_e32 v32, 0x14a0, v3
	s_waitcnt vmcnt(2)
	ds_write2_b32 v32, v56, v57 offset1:1
	v_add_u32_e32 v32, 0x14a8, v3
	ds_write2_b32 v32, v58, v59 offset1:1
	v_add_u32_e32 v32, 0x18c0, v3
	s_waitcnt vmcnt(1)
	ds_write2_b32 v32, v60, v61 offset1:1
	v_add_u32_e32 v32, 0x18c8, v3
	ds_write2_b32 v32, v62, v63 offset1:1
	v_add_u32_e32 v32, 0x1ce0, v3
	v_add_u32_e32 v3, 0x1ce8, v3
	s_waitcnt vmcnt(0)
	ds_write2_b32 v32, v64, v65 offset1:1
	ds_write2_b32 v3, v66, v67 offset1:1
	s_waitcnt lgkmcnt(0)
	ds_read2_b32 v[34:35], v50 offset1:8
	ds_read2_b32 v[36:37], v50 offset0:33 offset1:41
	ds_read2_b32 v[44:45], v50 offset0:132 offset1:140
	ds_read2_b32 v[46:47], v50 offset0:165 offset1:173
	ds_read2_b32 v[38:39], v50 offset0:66 offset1:74
	ds_read2_b32 v[40:41], v50 offset0:99 offset1:107
	s_waitcnt lgkmcnt(5)
	v_mul_f32_e32 v3, 0x42000000, v34
	s_waitcnt lgkmcnt(4)
	v_mul_f32_e32 v34, 0x42000000, v36
	v_med3_f32 v3, v3, s83, v238
	v_med3_f32 v34, v34, s83, v238
	ds_read2_b32 v[48:49], v50 offset0:198 offset1:206
	ds_read2_b32 v[52:53], v50 offset0:231 offset1:239
	v_cvt_pk_fp8_f32 v42, v3, v34
	s_waitcnt lgkmcnt(5)
	v_mul_f32_e32 v3, 0x42000000, v44
	s_waitcnt lgkmcnt(4)
	v_mul_f32_e32 v34, 0x42000000, v46
	v_med3_f32 v3, v3, s83, v238
	v_med3_f32 v34, v34, s83, v238
	s_waitcnt lgkmcnt(3)
	v_mul_f32_e32 v36, 0x42000000, v38
	s_waitcnt lgkmcnt(2)
	v_mul_f32_e32 v38, 0x42000000, v40
	v_cvt_pk_fp8_f32 v43, v3, v34
	v_mul_f32_e32 v3, 0x42000000, v35
	v_mul_f32_e32 v34, 0x42000000, v37
	v_med3_f32 v36, v36, s83, v238
	v_med3_f32 v38, v38, s83, v238
	v_med3_f32 v3, v3, s83, v238
	v_med3_f32 v37, v34, s83, v238
	v_mov_b32_e32 v34, v0
	v_cvt_pk_fp8_f32 v42, v36, v38 op_sel:[0,0,1]
	s_waitcnt lgkmcnt(1)
	v_mul_f32_e32 v36, 0x42000000, v48
	s_waitcnt lgkmcnt(0)
	v_mul_f32_e32 v38, 0x42000000, v52
	v_cvt_pk_fp8_f32 v34, v3, v37
	v_med3_f32 v36, v36, s83, v238
	v_med3_f32 v38, v38, s83, v238
	v_cvt_pk_fp8_f32 v43, v36, v38 op_sel:[0,0,1]
	v_mul_f32_e32 v35, 0x42000000, v39
	v_mul_f32_e32 v36, 0x42000000, v41
	v_med3_f32 v35, v35, s83, v238
	v_med3_f32 v36, v36, s83, v238
	v_cvt_pk_fp8_f32 v34, v35, v36 op_sel:[0,0,1]
	v_mul_f32_e32 v3, 0x42000000, v45
	v_mul_f32_e32 v35, 0x42000000, v47
	v_med3_f32 v3, v3, s83, v238
	v_med3_f32 v38, v35, s83, v238
	v_mov_b32_e32 v35, v0
	v_cvt_pk_fp8_f32 v35, v3, v38
	v_mul_f32_e32 v36, 0x42000000, v49
	v_mul_f32_e32 v37, 0x42000000, v53
	v_med3_f32 v36, v36, s83, v238
	v_med3_f32 v37, v37, s83, v238
	v_cvt_pk_fp8_f32 v35, v36, v37 op_sel:[0,0,1]
	v_lshl_add_u64 v[32:33], s[8:9], 0, v[6:7]
	v_lshl_add_u64 v[36:37], v[32:33], 0, v[18:19]
	ds_read2_b32 v[44:45], v50 offset0:148 offset1:156
	global_store_dwordx2 v[36:37], v[34:35], off nt
	ds_read2_b32 v[34:35], v50 offset0:16 offset1:24
	ds_read2_b32 v[36:37], v50 offset0:49 offset1:57
	ds_read2_b32 v[46:47], v50 offset0:181 offset1:189
	ds_read2_b32 v[38:39], v50 offset0:82 offset1:90
	ds_read2_b32 v[40:41], v50 offset0:115 offset1:123
	v_lshl_add_u64 v[54:55], v[32:33], 0, v[16:17]
	s_waitcnt lgkmcnt(4)
; #define LAS __attribute__((address_space(3)))
; __device__ __forceinline__ void p0_transpose_item8(const float* W, int ldw, int srccol0, int k0, unsigned char* dst, int K, LAS float* scr, int lane) {
;     ...
;     const int c = lane & 7;
; #pragma unroll
;     for (int j = 0; j < 4; ++j) { const int n = (lane >> 3) + 8 * j; const LAS float* s = scr + (8 * c) * 33 + n;
;         u32x2 o; o.x = pk4_f8(s[0 * 33] * 32.f, s[1 * 33] * 32.f, s[2 * 33] * 32.f, s[3 * 33] * 32.f); o.y = pk4_f8(s[4 * 33] * 32.f, s[5 * 33] * 32.f, s[6 * 33] * 32.f, s[7 * 33] * 32.f);
;         *(u32x2*)(dst + (size_t)n * K + k0 + 8 * c) = o; }
; __device__ __forceinline__ void p0_item(KP Pk, Frame& F, int it, LAS float* scr) {
;     ...
;         if (r < TI_WA) { if (WIN_F8_L(l)) p0_transpose_item8(Pk->in[I_WIN] + (size_t)l * D * DIN, DIN, 1536, 64 * r, ws + WS_WA + (size_t)l * 32 * D * 2, D, scr, F.lane);
;             else p0_transpose_item(Pk->in[I_WIN] + (size_t)l * D * DIN, DIN, 1536, 64 * r, (bf16_t*)(ws + WS_WA) + (size_t)l * 32 * D, D, scr, F.lane); return; }
	v_mul_f32_e32 v3, 0x42000000, v34
	s_waitcnt lgkmcnt(3)
	v_mul_f32_e32 v34, 0x42000000, v36
	global_store_dwordx2 v[54:55], v[42:43], off nt
	v_med3_f32 v3, v3, s83, v238
	v_med3_f32 v34, v34, s83, v238
	v_mov_b32_e32 v42, v0
	ds_read2_b32 v[48:49], v50 offset0:214 offset1:222
	ds_read2_b32 v[52:53], v50 offset0:247 offset1:255
	v_cvt_pk_fp8_f32 v42, v3, v34
	v_mul_f32_e32 v3, 0x42000000, v44
	s_waitcnt lgkmcnt(4)
	v_mul_f32_e32 v34, 0x42000000, v46
	v_med3_f32 v3, v3, s83, v238
	v_med3_f32 v34, v34, s83, v238
	v_mov_b32_e32 v43, v0
	s_waitcnt lgkmcnt(3)
	v_mul_f32_e32 v36, 0x42000000, v38
	s_waitcnt lgkmcnt(2)
	v_mul_f32_e32 v38, 0x42000000, v40
	v_cvt_pk_fp8_f32 v43, v3, v34
	v_mul_f32_e32 v3, 0x42000000, v35
	v_mul_f32_e32 v34, 0x42000000, v37
	v_med3_f32 v36, v36, s83, v238
	v_med3_f32 v38, v38, s83, v238
	v_med3_f32 v3, v3, s83, v238
	v_med3_f32 v37, v34, s83, v238
	v_mov_b32_e32 v34, v0
	v_cvt_pk_fp8_f32 v42, v36, v38 op_sel:[0,0,1]
	s_waitcnt lgkmcnt(1)
	v_mul_f32_e32 v36, 0x42000000, v48
	s_waitcnt lgkmcnt(0)
	v_mul_f32_e32 v38, 0x42000000, v52
	v_cvt_pk_fp8_f32 v34, v3, v37
	v_med3_f32 v36, v36, s83, v238
	v_med3_f32 v38, v38, s83, v238
	v_cvt_pk_fp8_f32 v43, v36, v38 op_sel:[0,0,1]
	v_mul_f32_e32 v35, 0x42000000, v39
	v_mul_f32_e32 v36, 0x42000000, v41
	v_med3_f32 v35, v35, s83, v238
	v_med3_f32 v36, v36, s83, v238
	v_cvt_pk_fp8_f32 v34, v35, v36 op_sel:[0,0,1]
	v_mul_f32_e32 v3, 0x42000000, v45
	v_mul_f32_e32 v35, 0x42000000, v47
	v_med3_f32 v3, v3, s83, v238
	v_med3_f32 v38, v35, s83, v238
	v_mov_b32_e32 v35, v0
	v_cvt_pk_fp8_f32 v35, v3, v38
	v_mul_f32_e32 v36, 0x42000000, v49
	v_mul_f32_e32 v37, 0x42000000, v53
	v_med3_f32 v36, v36, s83, v238
	v_med3_f32 v37, v37, s83, v238
	v_cvt_pk_fp8_f32 v35, v36, v37 op_sel:[0,0,1]
	v_lshl_add_u64 v[54:55], v[32:33], 0, v[20:21]
	v_lshl_add_u64 v[32:33], v[32:33], 0, v[22:23]
	global_store_dwordx2 v[54:55], v[42:43], off nt
	global_store_dwordx2 v[32:33], v[34:35], off nt
	s_waitcnt lgkmcnt(0)
	s_mov_b64 s[8:9], 0
.LBB0_844:
	s_andn2_b64 vcc, exec, s[8:9]
	s_cbranch_vccnz .LBB0_849
	s_lshl_b32 s5, s4, 6
	s_add_i32 s8, s5, 0xfffac000
	s_waitcnt lgkmcnt(0)
	s_load_dwordx2 s[26:27], s[48:49], 0x40
	v_add_u32_e32 v3, s8, v2
	v_add_u32_e32 v32, 8, v3
	v_mad_i64_i32 v[34:35], s[18:19], v32, s2, 0
	v_add_u32_e32 v32, 16, v3
	s_cmp_gt_u32 s60, 1
	v_mad_i64_i32 v[36:37], s[18:19], v3, s2, 0
	v_mad_i64_i32 v[32:33], s[18:19], v32, s2, 0
	s_mov_b64 s[34:35], -1
	v_add_u32_e32 v41, 24, v3
	v_add_u32_e32 v40, 32, v3
	v_add_u32_e32 v39, 40, v3
	v_add_u32_e32 v38, 48, v3
	v_add_u32_e32 v3, 56, v3
	s_cbranch_scc1 .LBB0_847
	s_mul_i32 s9, s60, 0x2a40000
	s_mul_hi_u32 s5, s60, 0x2a40000
	s_waitcnt lgkmcnt(0)
	s_add_u32 s18, s26, s9
	s_addc_u32 s19, s27, s5
	v_lshlrev_b32_e32 v42, 2, v4
	v_mov_b32_e32 v43, v0
	v_lshl_add_u64 v[42:43], s[18:19], 0, v[42:43]
	s_mov_b64 s[18:19], 0x1800
	v_lshl_add_u64 v[72:73], v[42:43], 0, s[18:19]
	v_lshl_add_u64 v[42:43], v[72:73], 0, v[36:37]
	v_lshl_add_u64 v[46:47], v[72:73], 0, v[34:35]
	v_lshl_add_u64 v[52:53], v[72:73], 0, v[32:33]
	v_mad_i64_i32 v[56:57], s[18:19], v41, s2, v[72:73]
	v_mad_i64_i32 v[60:61], s[18:19], v40, s2, v[72:73]
	v_mad_i64_i32 v[64:65], s[18:19], v39, s2, v[72:73]
	global_load_dwordx4 v[42:45], v[42:43], off nt
	s_nop 0
	global_load_dwordx4 v[46:49], v[46:47], off nt
	s_nop 0
	global_load_dwordx4 v[52:55], v[52:53], off nt
	s_nop 0
	global_load_dwordx4 v[56:59], v[56:57], off nt
	s_nop 0
	global_load_dwordx4 v[60:63], v[60:61], off nt
	s_nop 0
	global_load_dwordx4 v[64:67], v[64:65], off nt
	v_mad_i64_i32 v[68:69], s[18:19], v38, s2, v[72:73]
	global_load_dwordx4 v[68:71], v[68:69], off nt
	v_mad_i64_i32 v[72:73], s[18:19], v3, s2, v[72:73]
	global_load_dwordx4 v[72:75], v[72:73], off nt
	v_add_u32_e32 v51, v1, v5
	v_add_u32_e32 v82, 0x420, v51
	v_add_u32_e32 v83, 0x428, v51
	v_add_u32_e32 v84, 0x840, v51
	v_add_u32_e32 v85, 0x848, v51
	v_add_u32_e32 v86, 0xc60, v51
	v_add_u32_e32 v87, 0xc68, v51
	v_add_u32_e32 v88, 0x1080, v51
	v_add_u32_e32 v89, 0x1088, v51
	v_add_u32_e32 v90, 0x14a0, v51
	v_add_u32_e32 v91, 0x14a8, v51
	v_add_u32_e32 v92, 0x18c0, v51
	v_add_u32_e32 v93, 0x18c8, v51
	v_add_u32_e32 v94, 0x1ce0, v51
	v_add_u32_e32 v95, 0x1ce8, v51
	v_mov_b32_e32 v77, v0
	v_mov_b32_e32 v76, v0
	s_lshl_b64 s[18:19], s[60:61], 17
	v_readlane_b32 s5, v255, 13
	s_add_u32 s5, s5, s18
	v_readlane_b32 s9, v255, 14
	s_addc_u32 s9, s9, s19
	s_add_u32 s18, s5, s8
	s_addc_u32 s19, s9, 0
	v_lshl_add_u64 v[78:79], s[18:19], 0, v[6:7]
	v_lshl_add_u64 v[80:81], v[78:79], 0, v[16:17]
	s_mov_b64 s[34:35], 0
	s_waitcnt vmcnt(7)
	ds_write2_b32 v51, v42, v43 offset1:1
	ds_write2_b32 v51, v44, v45 offset0:2 offset1:3
	s_waitcnt vmcnt(6)
	ds_write2_b32 v82, v46, v47 offset1:1
	ds_write2_b32 v83, v48, v49 offset1:1
	s_waitcnt vmcnt(5)
	ds_write2_b32 v84, v52, v53 offset1:1
	ds_write2_b32 v85, v54, v55 offset1:1
	s_waitcnt vmcnt(4)
	ds_write2_b32 v86, v56, v57 offset1:1
	ds_write2_b32 v87, v58, v59 offset1:1
	s_waitcnt vmcnt(3)
	ds_write2_b32 v88, v60, v61 offset1:1
	ds_write2_b32 v89, v62, v63 offset1:1
	s_waitcnt vmcnt(2)
	ds_write2_b32 v90, v64, v65 offset1:1
	ds_write2_b32 v91, v66, v67 offset1:1
	s_waitcnt vmcnt(1)
	ds_write2_b32 v92, v68, v69 offset1:1
	ds_write2_b32 v93, v70, v71 offset1:1
	s_waitcnt vmcnt(0)
	ds_write2_b32 v94, v72, v73 offset1:1
	ds_write2_b32 v95, v74, v75 offset1:1
	s_waitcnt lgkmcnt(0)
	ds_read2_b32 v[42:43], v50 offset1:8
	ds_read2_b32 v[44:45], v50 offset0:33 offset1:41
	ds_read2_b32 v[46:47], v50 offset0:66 offset1:74
	ds_read2_b32 v[48:49], v50 offset0:99 offset1:107
	ds_read2_b32 v[52:53], v50 offset0:132 offset1:140
	ds_read2_b32 v[54:55], v50 offset0:165 offset1:173
	ds_read2_b32 v[56:57], v50 offset0:198 offset1:206
	ds_read2_b32 v[58:59], v50 offset0:231 offset1:239
	s_waitcnt lgkmcnt(7)
; #define LAS __attribute__((address_space(3)))
; __device__ __forceinline__ void p0_transpose_item(const float* W, int ldw, int srccol0, int k0, bf16_t* dst, int K, LAS float* scr, int lane, bool q = false) {
;     { f32x4 v[8];
; #pragma unroll
;       for (int i = 0; i < 8; ++i) v[i] = *(const f32x4*)(W + (size_t)(k0 + 8 * i + (lane >> 3)) * ldw + srccol0 + 4 * (lane & 7));
; __device__ __forceinline__ void p0_transpose_item8(const float* W, int ldw, int srccol0, int k0, unsigned char* dst, int K, LAS float* scr, int lane) {
;     ...
;     const int c = lane & 7;
; #pragma unroll
;     for (int j = 0; j < 4; ++j) { const int n = (lane >> 3) + 8 * j; const LAS float* s = scr + (8 * c) * 33 + n;
;         u32x2 o; o.x = pk4_f8(s[0 * 33] * 32.f, s[1 * 33] * 32.f, s[2 * 33] * 32.f, s[3 * 33] * 32.f); o.y = pk4_f8(s[4 * 33] * 32.f, s[5 * 33] * 32.f, s[6 * 33] * 32.f, s[7 * 33] * 32.f);
;         *(u32x2*)(dst + (size_t)n * K + k0 + 8 * c) = o; }
	v_mul_f32_e32 v42, 0x42000000, v42
	s_waitcnt lgkmcnt(3)
	v_mul_f32_e32 v51, 0x42000000, v52
	s_waitcnt lgkmcnt(2)
	v_mul_f32_e32 v52, 0x42000000, v54
	v_med3_f32 v51, v51, s83, v238
	v_med3_f32 v52, v52, s83, v238
	v_cvt_pk_fp8_f32 v77, v51, v52
	v_mul_f32_e32 v44, 0x42000000, v44
	s_waitcnt lgkmcnt(1)
	v_mul_f32_e32 v54, 0x42000000, v56
	s_waitcnt lgkmcnt(0)
	v_mul_f32_e32 v56, 0x42000000, v58
	v_med3_f32 v42, v42, s83, v238
	v_med3_f32 v44, v44, s83, v238
	v_mul_f32_e32 v43, 0x42000000, v43
	v_mul_f32_e32 v45, 0x42000000, v45
	v_cvt_pk_fp8_f32 v76, v42, v44
	v_med3_f32 v42, v54, s83, v238
	v_med3_f32 v44, v56, s83, v238
	v_cvt_pk_fp8_f32 v77, v42, v44 op_sel:[0,0,1]
	v_med3_f32 v43, v43, s83, v238
	v_med3_f32 v45, v45, s83, v238
	v_mov_b32_e32 v42, v0
	v_cvt_pk_fp8_f32 v42, v43, v45
	v_mul_f32_e32 v44, 0x42000000, v47
	v_mul_f32_e32 v43, 0x42000000, v49
	v_mul_f32_e32 v46, 0x42000000, v46
	v_mul_f32_e32 v48, 0x42000000, v48
	v_med3_f32 v44, v44, s83, v238
	v_med3_f32 v43, v43, s83, v238
	v_med3_f32 v46, v46, s83, v238
	v_med3_f32 v48, v48, s83, v238
	v_cvt_pk_fp8_f32 v42, v44, v43 op_sel:[0,0,1]
	v_mul_f32_e32 v43, 0x42000000, v53
	v_mul_f32_e32 v44, 0x42000000, v55
	v_cvt_pk_fp8_f32 v76, v46, v48 op_sel:[0,0,1]
	v_med3_f32 v46, v43, s83, v238
	v_med3_f32 v44, v44, s83, v238
	v_mov_b32_e32 v43, v0
	v_cvt_pk_fp8_f32 v43, v46, v44
	v_mul_f32_e32 v45, 0x42000000, v57
	v_mul_f32_e32 v44, 0x42000000, v59
	v_med3_f32 v45, v45, s83, v238
	v_med3_f32 v44, v44, s83, v238
	global_store_dwordx2 v[80:81], v[76:77], off nt
	v_cvt_pk_fp8_f32 v43, v45, v44 op_sel:[0,0,1]
	ds_read2_b32 v[46:47], v50 offset0:16 offset1:24
	ds_read2_b32 v[48:49], v50 offset0:49 offset1:57
	ds_read2_b32 v[52:53], v50 offset0:82 offset1:90
	ds_read2_b32 v[54:55], v50 offset0:115 offset1:123
	v_lshl_add_u64 v[44:45], v[78:79], 0, v[18:19]
	global_store_dwordx2 v[44:45], v[42:43], off nt
	s_waitcnt lgkmcnt(3)
	v_mul_f32_e32 v42, 0x42000000, v46
	s_waitcnt lgkmcnt(2)
	v_mul_f32_e32 v43, 0x42000000, v48
	s_waitcnt lgkmcnt(1)
	v_mul_f32_e32 v44, 0x42000000, v52
	v_med3_f32 v45, v42, s83, v238
	v_med3_f32 v43, v43, s83, v238
	v_mov_b32_e32 v42, v0
	v_med3_f32 v48, v44, s83, v238
	v_cvt_pk_fp8_f32 v42, v45, v43
	ds_read2_b32 v[44:45], v50 offset0:148 offset1:156
	ds_read2_b32 v[56:57], v50 offset0:181 offset1:189
	ds_read2_b32 v[58:59], v50 offset0:214 offset1:222
	s_waitcnt lgkmcnt(3)
	v_mul_f32_e32 v46, 0x42000000, v54
	v_med3_f32 v43, v46, s83, v238
	ds_read2_b32 v[60:61], v50 offset0:247 offset1:255
	v_cvt_pk_fp8_f32 v42, v48, v43 op_sel:[0,0,1]
	s_waitcnt lgkmcnt(3)
	v_mul_f32_e32 v43, 0x42000000, v44
	s_waitcnt lgkmcnt(2)
	v_mul_f32_e32 v44, 0x42000000, v56
	v_med3_f32 v48, v43, s83, v238
	v_med3_f32 v44, v44, s83, v238
	v_mov_b32_e32 v43, v0
	v_cvt_pk_fp8_f32 v43, v48, v44
	s_waitcnt lgkmcnt(1)
	v_mul_f32_e32 v46, 0x42000000, v58
	s_waitcnt lgkmcnt(0)
	v_mul_f32_e32 v44, 0x42000000, v60
	v_med3_f32 v46, v46, s83, v238
	v_med3_f32 v44, v44, s83, v238
	v_cvt_pk_fp8_f32 v43, v46, v44 op_sel:[0,0,1]
	v_mul_f32_e32 v44, 0x42000000, v47
	v_mul_f32_e32 v46, 0x42000000, v49
	v_med3_f32 v48, v44, s83, v238
	v_med3_f32 v46, v46, s83, v238
	v_mov_b32_e32 v44, v0
	v_cvt_pk_fp8_f32 v44, v48, v46
	v_mul_f32_e32 v47, 0x42000000, v53
	v_mul_f32_e32 v46, 0x42000000, v55
	v_med3_f32 v47, v47, s83, v238
	v_med3_f32 v46, v46, s83, v238
	v_cvt_pk_fp8_f32 v44, v47, v46 op_sel:[0,0,1]
	v_mul_f32_e32 v45, 0x42000000, v45
	v_mul_f32_e32 v46, 0x42000000, v57
	v_med3_f32 v48, v45, s83, v238
	v_med3_f32 v46, v46, s83, v238
	v_mov_b32_e32 v45, v0
	v_cvt_pk_fp8_f32 v45, v48, v46
	v_mul_f32_e32 v47, 0x42000000, v59
	v_mul_f32_e32 v46, 0x42000000, v61
	v_med3_f32 v47, v47, s83, v238
	v_med3_f32 v46, v46, s83, v238
	v_cvt_pk_fp8_f32 v45, v47, v46 op_sel:[0,0,1]
	v_lshl_add_u64 v[46:47], v[78:79], 0, v[20:21]
	global_store_dwordx2 v[46:47], v[42:43], off nt
	v_lshl_add_u64 v[42:43], v[78:79], 0, v[22:23]
	global_store_dwordx2 v[42:43], v[44:45], off nt
	s_waitcnt lgkmcnt(0)
.LBB0_847:
	s_andn2_b64 vcc, exec, s[34:35]
	s_cbranch_vccnz .LBB0_849
	s_ashr_i32 s19, s60, 31
	s_mul_i32 s9, s60, 0x2a40000
	s_mul_hi_i32 s5, s60, 0x2a40000
	s_waitcnt lgkmcnt(0)
	s_add_u32 s26, s26, s9
	s_addc_u32 s27, s27, s5
	v_lshlrev_b32_e32 v42, 2, v4
	v_mov_b32_e32 v43, v0
	v_lshl_add_u64 v[42:43], s[26:27], 0, v[42:43]
	s_mov_b64 s[26:27], 0x1800
	v_lshl_add_u64 v[64:65], v[42:43], 0, s[26:27]
	v_lshl_add_u64 v[36:37], v[64:65], 0, v[36:37]
	v_lshl_add_u64 v[34:35], v[64:65], 0, v[34:35]
	global_load_dwordx4 v[42:45], v[36:37], off nt
	v_lshl_add_u64 v[32:33], v[64:65], 0, v[32:33]
	global_load_dwordx4 v[34:37], v[34:35], off nt
	s_mov_b32 s18, s60
	global_load_dwordx4 v[46:49], v[32:33], off nt
	v_mad_i64_i32 v[32:33], s[26:27], v41, s2, v[64:65]
	global_load_dwordx4 v[52:55], v[32:33], off nt
	v_mad_i64_i32 v[32:33], s[26:27], v40, s2, v[64:65]
	global_load_dwordx4 v[56:59], v[32:33], off nt
	v_mad_i64_i32 v[32:33], s[26:27], v39, s2, v[64:65]
	global_load_dwordx4 v[60:63], v[32:33], off nt
	v_mad_i64_i32 v[32:33], s[26:27], v38, s2, v[64:65]
	global_load_dwordx4 v[38:41], v[32:33], off nt
	v_mad_i64_i32 v[32:33], s[26:27], v3, s2, v[64:65]
	global_load_dwordx4 v[64:67], v[32:33], off nt
	v_add_u32_e32 v3, v1, v5
	v_add_u32_e32 v32, 0x420, v3
	s_lshl_b64 s[18:19], s[18:19], 17
	v_readlane_b32 s5, v255, 13
	s_add_u32 s5, s5, s18
	v_readlane_b32 s9, v255, 14
	s_addc_u32 s18, s9, s19
	s_mov_b32 s9, s61
	s_lshl_b64 s[8:9], s[8:9], 1
	s_add_u32 s8, s5, s8
	s_addc_u32 s9, s18, s9
	v_mov_b32_e32 v33, v0
	s_waitcnt vmcnt(7)
; #define LAS __attribute__((address_space(3)))
; __device__ __forceinline__ unsigned pk2(float lo, float hi) { return f2bf(lo) | (f2bf(hi) << 16); }
; __device__ __forceinline__ unsigned pk2q(float lo, float hi) { return f2bf(q8(lo)) | (f2bf(q8(hi)) << 16); }
; #define LDS_WAIT() asm volatile("s_waitcnt lgkmcnt(0)" ::: "memory")
; __device__ __forceinline__ void p0_transpose_item(const float* W, int ldw, int srccol0, int k0, bf16_t* dst, int K, LAS float* scr, int lane, bool q = false) {
;     ...
;     LDS_WAIT(); asm volatile("" ::: "memory");
;     const int c = lane & 7;
; #pragma unroll
;     for (int j = 0; j < 4; ++j) { const int n = (lane >> 3) + 8 * j; const LAS float* s = scr + (8 * c) * 33 + n;
;         u32x4 o; if (q) { o.x = pk2q(s[0 * 33], s[1 * 33]); o.y = pk2q(s[2 * 33], s[3 * 33]); o.z = pk2q(s[4 * 33], s[5 * 33]); o.w = pk2q(s[6 * 33], s[7 * 33]); }
;         else { o.x = pk2(s[0 * 33], s[1 * 33]); o.y = pk2(s[2 * 33], s[3 * 33]); o.z = pk2(s[4 * 33], s[5 * 33]); o.w = pk2(s[6 * 33], s[7 * 33]); }
;         *(u32x4*)(dst + (size_t)n * K + k0 + 8 * c) = o; }
;     LDS_WAIT(); asm volatile("" ::: "memory");
; }
	ds_write2_b32 v3, v42, v43 offset1:1
	ds_write2_b32 v3, v44, v45 offset0:2 offset1:3
	s_waitcnt vmcnt(6)
	ds_write2_b32 v32, v34, v35 offset1:1
	v_add_u32_e32 v32, 0x428, v3
	ds_write2_b32 v32, v36, v37 offset1:1
	v_add_u32_e32 v32, 0x840, v3
	s_waitcnt vmcnt(5)
	ds_write2_b32 v32, v46, v47 offset1:1
	v_add_u32_e32 v32, 0x848, v3
	ds_write2_b32 v32, v48, v49 offset1:1
	v_add_u32_e32 v32, 0xc60, v3
	s_waitcnt vmcnt(4)
	ds_write2_b32 v32, v52, v53 offset1:1
	v_add_u32_e32 v32, 0xc68, v3
	ds_write2_b32 v32, v54, v55 offset1:1
	v_add_u32_e32 v32, 0x1080, v3
	s_waitcnt vmcnt(3)
	ds_write2_b32 v32, v56, v57 offset1:1
	v_add_u32_e32 v32, 0x1088, v3
	ds_write2_b32 v32, v58, v59 offset1:1
	v_add_u32_e32 v32, 0x14a0, v3
	s_waitcnt vmcnt(2)
	ds_write2_b32 v32, v60, v61 offset1:1
	v_add_u32_e32 v32, 0x14a8, v3
	ds_write2_b32 v32, v62, v63 offset1:1
	v_add_u32_e32 v32, 0x18c0, v3
	s_waitcnt vmcnt(1)
	ds_write2_b32 v32, v38, v39 offset1:1
	v_add_u32_e32 v32, 0x18c8, v3
	ds_write2_b32 v32, v40, v41 offset1:1
	v_add_u32_e32 v32, 0x1ce0, v3
	v_add_u32_e32 v3, 0x1ce8, v3
	s_waitcnt vmcnt(0)
	ds_write2_b32 v32, v64, v65 offset1:1
	ds_write2_b32 v3, v66, v67 offset1:1
	s_waitcnt lgkmcnt(0)
	ds_read2_b32 v[38:39], v50 offset0:33 offset1:41
	ds_read2_b32 v[40:41], v50 offset1:8
	ds_read2_b32 v[42:43], v50 offset0:66 offset1:74
	ds_read2_b32 v[44:45], v50 offset0:99 offset1:107
	ds_read2_b32 v[46:47], v50 offset0:132 offset1:140
	ds_read2_b32 v[48:49], v50 offset0:165 offset1:173
	ds_read2_b32 v[52:53], v50 offset0:198 offset1:206
	ds_read2_b32 v[54:55], v50 offset0:231 offset1:239
	s_waitcnt lgkmcnt(7)
	v_bfe_u32 v34, v38, 16, 1
	s_waitcnt lgkmcnt(6)
	v_bfe_u32 v3, v40, 16, 1
	v_add3_u32 v3, v40, v3, s23
	v_lshrrev_b32_e32 v3, 16, v3
	v_add3_u32 v34, v38, v34, s23
	v_and_or_b32 v34, v34, s95, v3
	s_waitcnt lgkmcnt(5)
	v_bfe_u32 v3, v42, 16, 1
	v_add3_u32 v3, v42, v3, s23
	s_waitcnt lgkmcnt(4)
	v_bfe_u32 v35, v44, 16, 1
	v_lshrrev_b32_e32 v3, 16, v3
	v_add3_u32 v35, v44, v35, s23
	v_and_or_b32 v35, v35, s95, v3
	s_waitcnt lgkmcnt(3)
	v_bfe_u32 v3, v46, 16, 1
	v_add3_u32 v3, v46, v3, s23
	s_waitcnt lgkmcnt(2)
	v_bfe_u32 v36, v48, 16, 1
	v_lshrrev_b32_e32 v3, 16, v3
	v_add3_u32 v36, v48, v36, s23
	v_and_or_b32 v36, v36, s95, v3
	s_waitcnt lgkmcnt(1)
	v_bfe_u32 v3, v52, 16, 1
	v_lshlrev_b32_e32 v32, 1, v6
	v_add3_u32 v3, v52, v3, s23
	s_waitcnt lgkmcnt(0)
	v_bfe_u32 v37, v54, 16, 1
	v_lshl_add_u64 v[32:33], s[8:9], 0, v[32:33]
	v_lshrrev_b32_e32 v3, 16, v3
	v_add3_u32 v37, v54, v37, s23
	v_and_or_b32 v37, v37, s95, v3
	v_lshl_add_u64 v[56:57], v[32:33], 0, v[24:25]
	v_bfe_u32 v3, v41, 16, 1
	global_store_dwordx4 v[56:57], v[34:37], off nt
	v_add3_u32 v3, v41, v3, s23
	v_lshrrev_b32_e32 v3, 16, v3
	v_bfe_u32 v34, v39, 16, 1
	v_add3_u32 v34, v39, v34, s23
	v_and_or_b32 v34, v34, s95, v3
	v_bfe_u32 v3, v43, 16, 1
	v_add3_u32 v3, v43, v3, s23
	v_bfe_u32 v35, v45, 16, 1
	v_lshrrev_b32_e32 v3, 16, v3
	v_add3_u32 v35, v45, v35, s23
	v_and_or_b32 v35, v35, s95, v3
	v_bfe_u32 v3, v47, 16, 1
	v_add3_u32 v3, v47, v3, s23
	v_bfe_u32 v36, v49, 16, 1
	v_lshrrev_b32_e32 v3, 16, v3
	v_add3_u32 v36, v49, v36, s23
	v_and_or_b32 v36, v36, s95, v3
	v_bfe_u32 v3, v53, 16, 1
	v_add3_u32 v3, v53, v3, s23
	v_bfe_u32 v37, v55, 16, 1
	v_lshrrev_b32_e32 v3, 16, v3
	v_add3_u32 v37, v55, v37, s23
	v_and_or_b32 v37, v37, s95, v3
	v_lshl_add_u64 v[38:39], v[32:33], 0, v[26:27]
	global_store_dwordx4 v[38:39], v[34:37], off nt
	ds_read2_b32 v[38:39], v50 offset0:49 offset1:57
	ds_read2_b32 v[40:41], v50 offset0:16 offset1:24
	ds_read2_b32 v[42:43], v50 offset0:82 offset1:90
	ds_read2_b32 v[44:45], v50 offset0:115 offset1:123
	ds_read2_b32 v[46:47], v50 offset0:148 offset1:156
	ds_read2_b32 v[48:49], v50 offset0:181 offset1:189
	ds_read2_b32 v[52:53], v50 offset0:214 offset1:222
	ds_read2_b32 v[54:55], v50 offset0:247 offset1:255
	s_waitcnt lgkmcnt(7)
	v_bfe_u32 v34, v38, 16, 1
	s_waitcnt lgkmcnt(6)
	v_bfe_u32 v3, v40, 16, 1
	v_add3_u32 v3, v40, v3, s23
	v_lshrrev_b32_e32 v3, 16, v3
	v_add3_u32 v34, v38, v34, s23
	v_and_or_b32 v34, v34, s95, v3
	s_waitcnt lgkmcnt(5)
	v_bfe_u32 v3, v42, 16, 1
	v_add3_u32 v3, v42, v3, s23
	s_waitcnt lgkmcnt(4)
	v_bfe_u32 v35, v44, 16, 1
	v_lshrrev_b32_e32 v3, 16, v3
	v_add3_u32 v35, v44, v35, s23
	v_and_or_b32 v35, v35, s95, v3
	s_waitcnt lgkmcnt(3)
	v_bfe_u32 v3, v46, 16, 1
	v_add3_u32 v3, v46, v3, s23
	s_waitcnt lgkmcnt(2)
	v_bfe_u32 v36, v48, 16, 1
	v_lshrrev_b32_e32 v3, 16, v3
	v_add3_u32 v36, v48, v36, s23
	v_and_or_b32 v36, v36, s95, v3
	s_waitcnt lgkmcnt(1)
	v_bfe_u32 v3, v52, 16, 1
	v_add3_u32 v3, v52, v3, s23
	s_waitcnt lgkmcnt(0)
	v_bfe_u32 v37, v54, 16, 1
	v_lshrrev_b32_e32 v3, 16, v3
	v_add3_u32 v37, v54, v37, s23
	v_and_or_b32 v37, v37, s95, v3
	v_lshl_add_u64 v[56:57], v[32:33], 0, v[28:29]
	v_bfe_u32 v3, v41, 16, 1
	global_store_dwordx4 v[56:57], v[34:37], off nt
	v_add3_u32 v3, v41, v3, s23
	v_lshrrev_b32_e32 v3, 16, v3
	v_bfe_u32 v34, v39, 16, 1
	v_add3_u32 v34, v39, v34, s23
	v_and_or_b32 v34, v34, s95, v3
	v_bfe_u32 v3, v43, 16, 1
	v_add3_u32 v3, v43, v3, s23
	v_bfe_u32 v35, v45, 16, 1
	v_lshrrev_b32_e32 v3, 16, v3
	v_add3_u32 v35, v45, v35, s23
	v_and_or_b32 v35, v35, s95, v3
	v_bfe_u32 v3, v47, 16, 1
	v_add3_u32 v3, v47, v3, s23
	v_bfe_u32 v36, v49, 16, 1
	v_lshrrev_b32_e32 v3, 16, v3
	v_add3_u32 v36, v49, v36, s23
	v_and_or_b32 v36, v36, s95, v3
	v_bfe_u32 v3, v53, 16, 1
	v_add3_u32 v3, v53, v3, s23
	v_bfe_u32 v37, v55, 16, 1
	v_lshrrev_b32_e32 v3, 16, v3
	v_add3_u32 v37, v55, v37, s23
	v_and_or_b32 v37, v37, s95, v3
	v_lshl_add_u64 v[32:33], v[32:33], 0, v[30:31]
	global_store_dwordx4 v[32:33], v[34:37], off nt
	s_waitcnt lgkmcnt(0)

; #define LAS __attribute__((address_space(3)))
; #define LDS_WAIT() asm volatile("s_waitcnt lgkmcnt(0)" ::: "memory")
; __device__ __forceinline__ void p0_transpose_item8(const float* W, int ldw, int srccol0, int k0, unsigned char* dst, int K, LAS float* scr, int lane) {
;     { f32x4 v[8];
; #pragma unroll
;       for (int i = 0; i < 8; ++i) v[i] = *(const f32x4*)(W + (size_t)(k0 + 8 * i + (lane >> 3)) * ldw + srccol0 + 4 * (lane & 7));
; #pragma unroll
;       for (int i = 0; i < 8; ++i) { LAS float* p = scr + (8 * i + (lane >> 3)) * 33 + 4 * (lane & 7); p[0] = v[i][0]; p[1] = v[i][1]; p[2] = v[i][2]; p[3] = v[i][3]; } }
;     LDS_WAIT(); asm volatile("" ::: "memory");
;     const int c = lane & 7;
; #pragma unroll
;     for (int j = 0; j < 4; ++j) { const int n = (lane >> 3) + 8 * j; const LAS float* s = scr + (8 * c) * 33 + n;
;         u32x2 o; o.x = pk4_f8(s[0 * 33] * 32.f, s[1 * 33] * 32.f, s[2 * 33] * 32.f, s[3 * 33] * 32.f); o.y = pk4_f8(s[4 * 33] * 32.f, s[5 * 33] * 32.f, s[6 * 33] * 32.f, s[7 * 33] * 32.f);
;         *(u32x2*)(dst + (size_t)n * K + k0 + 8 * c) = o; }
; __device__ __forceinline__ void p0_item(KP Pk, Frame& F, int it, LAS float* scr) {
;     ...
;         if (r < TI_WIN) { const int kb = r / 168, nb = r % 168, n0 = 32 * nb;
;             if (WIN_F8_L(l)) p0_transpose_item8(Pk->in[I_WIN] + (size_t)l * D * DIN, DIN, n0 < 1536 ? n0 : n0 + 32, 64 * kb, ws + WS_WIN + (size_t)l * NU * D * 2 + (size_t)n0 * D, D, scr, F.lane);
;             else p0_transpose_item(Pk->in[I_WIN] + (size_t)l * D * DIN, DIN, n0 < 1536 ? n0 : n0 + 32, 64 * kb, (bf16_t*)(ws + WS_WIN) + ((size_t)l * NU + n0) * D, D, scr, F.lane); return; }
.LBB0_850:
	s_andn2_b64 vcc, exec, s[8:9]
	s_cbranch_vccnz .LBB0_819
	s_mul_i32 s5, s4, 0xffffc30d
	s_lshr_b32 s5, s5, 16
	s_add_i32 s5, s5, s4
	s_sext_i32_i16 s8, s5
	s_ashr_i32 s8, s8, 7
	s_bfe_u32 s5, s5, 0x1000f
	s_add_i32 s5, s8, s5
	s_sext_i32_i16 s8, s5
	s_mulk_i32 s5, 0xa8
	s_sub_i32 s4, s4, s5
	s_sext_i32_i16 s4, s4
	s_lshl_b32 s34, s4, 5
	s_add_i32 s5, s34, 32
	s_cmp_lt_i32 s4, 48
	s_waitcnt lgkmcnt(0)
	s_cselect_b32 s26, s34, s5
	s_lshl_b32 s8, s8, 6
	s_load_dwordx2 s[38:39], s[48:49], 0x40
	v_add_u32_e32 v3, s8, v2
	v_add_u32_e32 v32, 8, v3
	s_ashr_i32 s27, s26, 31
	v_mad_i64_i32 v[34:35], s[4:5], v3, s2, 0
	v_mad_i64_i32 v[32:33], s[4:5], v32, s2, 0
	v_add_u32_e32 v62, 16, v3
	v_add_u32_e32 v61, 24, v3
	v_add_u32_e32 v60, 32, v3
	v_add_u32_e32 v59, 40, v3
	v_add_u32_e32 v58, 48, v3
	v_add_u32_e32 v57, 56, v3
	v_add_u32_e32 v3, v1, v5
	s_cmp_gt_u32 s60, 1
	s_mov_b64 s[40:41], -1
	s_mul_i32 s4, s60, 0x2a40000
	v_lshlrev_b32_e32 v36, 2, v4
	v_add_u32_e32 v42, 0x420, v3
	v_add_u32_e32 v43, 0x428, v3
	v_add_u32_e32 v44, 0x840, v3
	v_add_u32_e32 v45, 0x848, v3
	v_add_u32_e32 v46, 0xc60, v3
	v_add_u32_e32 v47, 0xc68, v3
	v_add_u32_e32 v48, 0x1080, v3
	v_add_u32_e32 v49, 0x1088, v3
	v_add_u32_e32 v51, 0x14a0, v3
	v_add_u32_e32 v52, 0x14a8, v3
	v_add_u32_e32 v53, 0x18c0, v3
	v_add_u32_e32 v54, 0x18c8, v3
	v_add_u32_e32 v55, 0x1ce0, v3
	v_add_u32_e32 v56, 0x1ce8, v3
	s_cbranch_scc1 .LBB0_853
	s_mul_hi_u32 s5, s60, 0x2a40000
	s_waitcnt lgkmcnt(0)
	s_add_u32 s9, s38, s4
	s_addc_u32 s5, s39, s5
	s_mul_i32 s19, s60, 0x1500000
	v_readlane_b32 s35, v255, 15
	s_mul_hi_u32 s18, s60, 0x1500000
	s_add_u32 s37, s35, s19
	v_readlane_b32 s19, v255, 16
	s_addc_u32 s40, s19, s18
	s_ashr_i32 s35, s34, 31
	s_lshl_b64 s[18:19], s[34:35], 11
	s_add_u32 s35, s37, s18
	s_addc_u32 s37, s40, s19
	s_lshl_b64 s[18:19], s[26:27], 2
	s_add_u32 s18, s9, s18
	s_addc_u32 s19, s5, s19
	v_mov_b32_e32 v37, v0
	v_lshl_add_u64 v[88:89], s[18:19], 0, v[36:37]
	v_lshl_add_u64 v[38:39], v[88:89], 0, v[34:35]
	global_load_dwordx4 v[38:41], v[38:39], off nt
	v_lshl_add_u64 v[64:65], v[88:89], 0, v[32:33]
	global_load_dwordx4 v[64:67], v[64:65], off nt
	v_mad_i64_i32 v[68:69], s[18:19], v62, s2, v[88:89]
	global_load_dwordx4 v[68:71], v[68:69], off nt
	v_mad_i64_i32 v[72:73], s[18:19], v61, s2, v[88:89]
	global_load_dwordx4 v[72:75], v[72:73], off nt
	v_mad_i64_i32 v[76:77], s[18:19], v60, s2, v[88:89]
	global_load_dwordx4 v[76:79], v[76:77], off nt
	v_mad_i64_i32 v[80:81], s[18:19], v59, s2, v[88:89]
	global_load_dwordx4 v[80:83], v[80:81], off nt
	v_mad_i64_i32 v[84:85], s[18:19], v58, s2, v[88:89]
	global_load_dwordx4 v[84:87], v[84:85], off nt
	v_mad_i64_i32 v[88:89], s[18:19], v57, s2, v[88:89]
	global_load_dwordx4 v[88:91], v[88:89], off nt
	s_ashr_i32 s5, s8, 31
	s_add_u32 s18, s35, s8
	s_addc_u32 s19, s37, s5
	s_mov_b64 s[40:41], 0
	s_waitcnt vmcnt(7)
	ds_write2_b32 v3, v38, v39 offset1:1
	ds_write2_b32 v3, v40, v41 offset0:2 offset1:3
	s_waitcnt vmcnt(6)
	ds_write2_b32 v42, v64, v65 offset1:1
	ds_write2_b32 v43, v66, v67 offset1:1
	s_waitcnt vmcnt(5)
	ds_write2_b32 v44, v68, v69 offset1:1
	ds_write2_b32 v45, v70, v71 offset1:1
	s_waitcnt vmcnt(4)
	ds_write2_b32 v46, v72, v73 offset1:1
	ds_write2_b32 v47, v74, v75 offset1:1
	s_waitcnt vmcnt(3)
	ds_write2_b32 v48, v76, v77 offset1:1
	ds_write2_b32 v49, v78, v79 offset1:1
	s_waitcnt vmcnt(2)
	ds_write2_b32 v51, v80, v81 offset1:1
	ds_write2_b32 v52, v82, v83 offset1:1
	s_waitcnt vmcnt(1)
	ds_write2_b32 v53, v84, v85 offset1:1
	ds_write2_b32 v54, v86, v87 offset1:1
	s_waitcnt vmcnt(0)
	ds_write2_b32 v55, v88, v89 offset1:1
	ds_write2_b32 v56, v90, v91 offset1:1
	s_waitcnt lgkmcnt(0)
	ds_read2_b32 v[40:41], v50 offset1:8
	ds_read2_b32 v[64:65], v50 offset0:33 offset1:41
	ds_read2_b32 v[72:73], v50 offset0:132 offset1:140
	ds_read2_b32 v[74:75], v50 offset0:165 offset1:173
	ds_read2_b32 v[66:67], v50 offset0:66 offset1:74
	ds_read2_b32 v[68:69], v50 offset0:99 offset1:107
	s_waitcnt lgkmcnt(5)
	v_mul_f32_e32 v37, 0x42000000, v40
	s_waitcnt lgkmcnt(4)
	v_mul_f32_e32 v40, 0x42000000, v64
	v_med3_f32 v37, v37, s83, v238
	v_med3_f32 v40, v40, s83, v238
	v_mov_b32_e32 v70, v0
	ds_read2_b32 v[76:77], v50 offset0:198 offset1:206
	ds_read2_b32 v[78:79], v50 offset0:231 offset1:239
	v_cvt_pk_fp8_f32 v70, v37, v40
	s_waitcnt lgkmcnt(5)
	v_mul_f32_e32 v37, 0x42000000, v72
	s_waitcnt lgkmcnt(4)
	v_mul_f32_e32 v40, 0x42000000, v74
	v_med3_f32 v37, v37, s83, v238
	v_med3_f32 v40, v40, s83, v238
	v_mov_b32_e32 v71, v0
	s_waitcnt lgkmcnt(3)
	v_mul_f32_e32 v63, 0x42000000, v66
	s_waitcnt lgkmcnt(2)
	v_mul_f32_e32 v64, 0x42000000, v68
	v_cvt_pk_fp8_f32 v71, v37, v40
	v_med3_f32 v63, v63, s83, v238
	v_med3_f32 v64, v64, s83, v238
	v_cvt_pk_fp8_f32 v70, v63, v64 op_sel:[0,0,1]
	s_waitcnt lgkmcnt(1)
	v_mul_f32_e32 v63, 0x42000000, v76
	s_waitcnt lgkmcnt(0)
	v_mul_f32_e32 v64, 0x42000000, v78
	v_med3_f32 v63, v63, s83, v238
	v_med3_f32 v64, v64, s83, v238
	v_mul_f32_e32 v37, 0x42000000, v41
	v_mul_f32_e32 v40, 0x42000000, v65
	v_cvt_pk_fp8_f32 v71, v63, v64 op_sel:[0,0,1]
	v_med3_f32 v37, v37, s83, v238
	v_med3_f32 v64, v40, s83, v238
	v_mov_b32_e32 v40, v0
	v_cvt_pk_fp8_f32 v40, v37, v64
	v_mul_f32_e32 v41, 0x42000000, v67
	v_mul_f32_e32 v63, 0x42000000, v69
	v_med3_f32 v41, v41, s83, v238
	v_med3_f32 v63, v63, s83, v238
	v_cvt_pk_fp8_f32 v40, v41, v63 op_sel:[0,0,1]
	v_mul_f32_e32 v37, 0x42000000, v73
	v_mul_f32_e32 v41, 0x42000000, v75
	v_med3_f32 v37, v37, s83, v238
	v_med3_f32 v65, v41, s83, v238
	v_mov_b32_e32 v41, v0
	v_cvt_pk_fp8_f32 v41, v37, v65
	v_mul_f32_e32 v63, 0x42000000, v77
	v_mul_f32_e32 v64, 0x42000000, v79
	v_med3_f32 v63, v63, s83, v238
	v_med3_f32 v64, v64, s83, v238
	v_cvt_pk_fp8_f32 v41, v63, v64 op_sel:[0,0,1]
	v_lshl_add_u64 v[38:39], s[18:19], 0, v[6:7]
	v_lshl_add_u64 v[64:65], v[38:39], 0, v[18:19]
	ds_read2_b32 v[72:73], v50 offset0:148 offset1:156
	global_store_dwordx2 v[64:65], v[40:41], off nt
	ds_read2_b32 v[40:41], v50 offset0:16 offset1:24
	ds_read2_b32 v[64:65], v50 offset0:49 offset1:57
	ds_read2_b32 v[74:75], v50 offset0:181 offset1:189
	ds_read2_b32 v[66:67], v50 offset0:82 offset1:90
	ds_read2_b32 v[68:69], v50 offset0:115 offset1:123
	v_lshl_add_u64 v[80:81], v[38:39], 0, v[16:17]
	s_waitcnt lgkmcnt(4)
; #define LAS __attribute__((address_space(3)))
; __device__ __forceinline__ void p0_transpose_item8(const float* W, int ldw, int srccol0, int k0, unsigned char* dst, int K, LAS float* scr, int lane) {
;     ...
;     const int c = lane & 7;
; #pragma unroll
;     for (int j = 0; j < 4; ++j) { const int n = (lane >> 3) + 8 * j; const LAS float* s = scr + (8 * c) * 33 + n;
;         u32x2 o; o.x = pk4_f8(s[0 * 33] * 32.f, s[1 * 33] * 32.f, s[2 * 33] * 32.f, s[3 * 33] * 32.f); o.y = pk4_f8(s[4 * 33] * 32.f, s[5 * 33] * 32.f, s[6 * 33] * 32.f, s[7 * 33] * 32.f);
;         *(u32x2*)(dst + (size_t)n * K + k0 + 8 * c) = o; }
	v_mul_f32_e32 v37, 0x42000000, v40
	s_waitcnt lgkmcnt(3)
	v_mul_f32_e32 v40, 0x42000000, v64
	global_store_dwordx2 v[80:81], v[70:71], off nt
	v_med3_f32 v37, v37, s83, v238
	v_med3_f32 v40, v40, s83, v238
	v_mov_b32_e32 v70, v0
	ds_read2_b32 v[76:77], v50 offset0:214 offset1:222
	ds_read2_b32 v[78:79], v50 offset0:247 offset1:255
	v_cvt_pk_fp8_f32 v70, v37, v40
	v_mul_f32_e32 v37, 0x42000000, v72
	s_waitcnt lgkmcnt(4)
	v_mul_f32_e32 v40, 0x42000000, v74
	v_med3_f32 v37, v37, s83, v238
	v_med3_f32 v40, v40, s83, v238
	v_mov_b32_e32 v71, v0
	s_waitcnt lgkmcnt(3)
	v_mul_f32_e32 v63, 0x42000000, v66
	s_waitcnt lgkmcnt(2)
	v_mul_f32_e32 v64, 0x42000000, v68
	v_cvt_pk_fp8_f32 v71, v37, v40
	v_med3_f32 v63, v63, s83, v238
	v_med3_f32 v64, v64, s83, v238
	v_cvt_pk_fp8_f32 v70, v63, v64 op_sel:[0,0,1]
	s_waitcnt lgkmcnt(1)
	v_mul_f32_e32 v63, 0x42000000, v76
	s_waitcnt lgkmcnt(0)
	v_mul_f32_e32 v64, 0x42000000, v78
	v_med3_f32 v63, v63, s83, v238
	v_med3_f32 v64, v64, s83, v238
	v_mul_f32_e32 v37, 0x42000000, v41
	v_mul_f32_e32 v40, 0x42000000, v65
	v_cvt_pk_fp8_f32 v71, v63, v64 op_sel:[0,0,1]
	v_med3_f32 v37, v37, s83, v238
	v_med3_f32 v64, v40, s83, v238
	v_mov_b32_e32 v40, v0
	v_cvt_pk_fp8_f32 v40, v37, v64
	v_mul_f32_e32 v41, 0x42000000, v67
	v_mul_f32_e32 v63, 0x42000000, v69
	v_med3_f32 v41, v41, s83, v238
	v_med3_f32 v63, v63, s83, v238
	v_cvt_pk_fp8_f32 v40, v41, v63 op_sel:[0,0,1]
	v_mul_f32_e32 v37, 0x42000000, v73
	v_mul_f32_e32 v41, 0x42000000, v75
	v_med3_f32 v37, v37, s83, v238
	v_med3_f32 v65, v41, s83, v238
	v_mov_b32_e32 v41, v0
	v_cvt_pk_fp8_f32 v41, v37, v65
	v_mul_f32_e32 v63, 0x42000000, v77
	v_mul_f32_e32 v64, 0x42000000, v79
	v_med3_f32 v63, v63, s83, v238
	v_med3_f32 v64, v64, s83, v238
	v_cvt_pk_fp8_f32 v41, v63, v64 op_sel:[0,0,1]
	v_lshl_add_u64 v[80:81], v[38:39], 0, v[20:21]
	v_lshl_add_u64 v[38:39], v[38:39], 0, v[22:23]
	global_store_dwordx2 v[80:81], v[70:71], off nt
	global_store_dwordx2 v[38:39], v[40:41], off nt
	s_waitcnt lgkmcnt(0)
; #define LAS __attribute__((address_space(3)))
; __device__ __forceinline__ unsigned pk2(float lo, float hi) { return f2bf(lo) | (f2bf(hi) << 16); }
; __device__ __forceinline__ unsigned pk2q(float lo, float hi) { return f2bf(q8(lo)) | (f2bf(q8(hi)) << 16); }
; #define LDS_WAIT() asm volatile("s_waitcnt lgkmcnt(0)" ::: "memory")
; __device__ __forceinline__ void p0_transpose_item(const float* W, int ldw, int srccol0, int k0, bf16_t* dst, int K, LAS float* scr, int lane, bool q = false) {
;     { f32x4 v[8];
; #pragma unroll
;       for (int i = 0; i < 8; ++i) v[i] = *(const f32x4*)(W + (size_t)(k0 + 8 * i + (lane >> 3)) * ldw + srccol0 + 4 * (lane & 7));
; #pragma unroll
;       for (int i = 0; i < 8; ++i) { LAS float* p = scr + (8 * i + (lane >> 3)) * 33 + 4 * (lane & 7); p[0] = v[i][0]; p[1] = v[i][1]; p[2] = v[i][2]; p[3] = v[i][3]; } }
;     LDS_WAIT(); asm volatile("" ::: "memory");
;     const int c = lane & 7;
; #pragma unroll
;     for (int j = 0; j < 4; ++j) { const int n = (lane >> 3) + 8 * j; const LAS float* s = scr + (8 * c) * 33 + n;
;         u32x4 o; if (q) { o.x = pk2q(s[0 * 33], s[1 * 33]); o.y = pk2q(s[2 * 33], s[3 * 33]); o.z = pk2q(s[4 * 33], s[5 * 33]); o.w = pk2q(s[6 * 33], s[7 * 33]); }
;         else { o.x = pk2(s[0 * 33], s[1 * 33]); o.y = pk2(s[2 * 33], s[3 * 33]); o.z = pk2(s[4 * 33], s[5 * 33]); o.w = pk2(s[6 * 33], s[7 * 33]); }
;         *(u32x4*)(dst + (size_t)n * K + k0 + 8 * c) = o; }
;     LDS_WAIT(); asm volatile("" ::: "memory");
; }
.LBB0_853:
	s_andn2_b64 vcc, exec, s[40:41]
	s_cbranch_vccnz .LBB0_819
	s_mul_hi_i32 s5, s60, 0x2a40000
	s_waitcnt lgkmcnt(0)
	s_add_u32 s9, s38, s4
	s_addc_u32 s18, s39, s5
	s_mul_i32 s4, s60, 0x1500
	s_ashr_i32 s19, s34, 31
	s_mul_hi_i32 s5, s60, 0x1500
	s_add_u32 s4, s4, s34
	s_addc_u32 s5, s5, s19
	s_lshl_b64 s[4:5], s[4:5], 12
	v_readlane_b32 s19, v255, 15
	s_add_u32 s19, s19, s4
	v_readlane_b32 s4, v255, 16
	s_addc_u32 s34, s4, s5
	s_lshl_b64 s[4:5], s[26:27], 2
	s_add_u32 s4, s9, s4
	s_addc_u32 s5, s18, s5
	v_mov_b32_e32 v37, v0
	v_lshl_add_u64 v[78:79], s[4:5], 0, v[36:37]
	v_lshl_add_u64 v[34:35], v[78:79], 0, v[34:35]
	global_load_dwordx4 v[34:37], v[34:35], off nt
	v_lshl_add_u64 v[32:33], v[78:79], 0, v[32:33]
	global_load_dwordx4 v[38:41], v[32:33], off nt
	v_mad_i64_i32 v[32:33], s[4:5], v62, s2, v[78:79]
	global_load_dwordx4 v[62:65], v[32:33], off nt
	v_mad_i64_i32 v[32:33], s[4:5], v61, s2, v[78:79]
	global_load_dwordx4 v[66:69], v[32:33], off nt
	v_mad_i64_i32 v[32:33], s[4:5], v60, s2, v[78:79]
	global_load_dwordx4 v[70:73], v[32:33], off nt
	v_mad_i64_i32 v[32:33], s[4:5], v59, s2, v[78:79]
	global_load_dwordx4 v[74:77], v[32:33], off nt
	v_mad_i64_i32 v[32:33], s[4:5], v58, s2, v[78:79]
	global_load_dwordx4 v[58:61], v[32:33], off nt
	v_mad_i64_i32 v[32:33], s[4:5], v57, s2, v[78:79]
	global_load_dwordx4 v[78:81], v[32:33], off nt
	s_ashr_i32 s9, s8, 31
	s_lshl_b64 s[4:5], s[8:9], 1
	s_add_u32 s8, s19, s4
	s_addc_u32 s9, s34, s5
	v_lshlrev_b32_e32 v32, 1, v6
	v_mov_b32_e32 v33, v0
	v_lshl_add_u64 v[32:33], s[8:9], 0, v[32:33]
	s_waitcnt vmcnt(7)
	ds_write2_b32 v3, v34, v35 offset1:1
	ds_write2_b32 v3, v36, v37 offset0:2 offset1:3
	s_waitcnt vmcnt(6)
	ds_write2_b32 v42, v38, v39 offset1:1
	ds_write2_b32 v43, v40, v41 offset1:1
	s_waitcnt vmcnt(5)
	ds_write2_b32 v44, v62, v63 offset1:1
	ds_write2_b32 v45, v64, v65 offset1:1
	s_waitcnt vmcnt(4)
	ds_write2_b32 v46, v66, v67 offset1:1
	ds_write2_b32 v47, v68, v69 offset1:1
	s_waitcnt vmcnt(3)
	ds_write2_b32 v48, v70, v71 offset1:1
	ds_write2_b32 v49, v72, v73 offset1:1
	s_waitcnt vmcnt(2)
	ds_write2_b32 v51, v74, v75 offset1:1
	ds_write2_b32 v52, v76, v77 offset1:1
	s_waitcnt vmcnt(1)
	ds_write2_b32 v53, v58, v59 offset1:1
	ds_write2_b32 v54, v60, v61 offset1:1
	s_waitcnt vmcnt(0)
	ds_write2_b32 v55, v78, v79 offset1:1
	ds_write2_b32 v56, v80, v81 offset1:1
	s_waitcnt lgkmcnt(0)
	ds_read2_b32 v[46:47], v50 offset0:33 offset1:41
	ds_read2_b32 v[48:49], v50 offset1:8
	v_lshl_add_u64 v[56:57], v[32:33], 0, v[24:25]
	s_waitcnt lgkmcnt(1)
	v_bfe_u32 v34, v46, 16, 1
	s_waitcnt lgkmcnt(0)
	v_bfe_u32 v3, v48, 16, 1
	v_add3_u32 v3, v48, v3, s23
	v_lshrrev_b32_e32 v3, 16, v3
	v_add3_u32 v34, v46, v34, s23
	v_and_or_b32 v52, v34, s95, v3
	ds_read2_b32 v[36:37], v50 offset0:66 offset1:74
	ds_read2_b32 v[34:35], v50 offset0:99 offset1:107
	ds_read2_b32 v[40:41], v50 offset0:132 offset1:140
	ds_read2_b32 v[38:39], v50 offset0:165 offset1:173
	ds_read2_b32 v[44:45], v50 offset0:198 offset1:206
	ds_read2_b32 v[42:43], v50 offset0:231 offset1:239
	s_waitcnt lgkmcnt(5)
	v_bfe_u32 v3, v36, 16, 1
	v_add3_u32 v3, v36, v3, s23
	s_waitcnt lgkmcnt(4)
	v_bfe_u32 v36, v34, 16, 1
	v_lshrrev_b32_e32 v3, 16, v3
	v_add3_u32 v34, v34, v36, s23
	v_and_or_b32 v53, v34, s95, v3
	s_waitcnt lgkmcnt(3)
	v_bfe_u32 v3, v40, 16, 1
	v_add3_u32 v3, v40, v3, s23
	s_waitcnt lgkmcnt(2)
	v_bfe_u32 v34, v38, 16, 1
	v_lshrrev_b32_e32 v3, 16, v3
	v_add3_u32 v34, v38, v34, s23
	v_and_or_b32 v54, v34, s95, v3
	s_waitcnt lgkmcnt(1)
	v_bfe_u32 v3, v44, 16, 1
	v_add3_u32 v3, v44, v3, s23
	s_waitcnt lgkmcnt(0)
	v_bfe_u32 v34, v42, 16, 1
	v_lshrrev_b32_e32 v3, 16, v3
	v_add3_u32 v34, v42, v34, s23
	v_and_or_b32 v55, v34, s95, v3
	v_bfe_u32 v3, v49, 16, 1
	v_add3_u32 v3, v49, v3, s23
	v_bfe_u32 v34, v47, 16, 1
	v_lshrrev_b32_e32 v3, 16, v3
	v_add3_u32 v34, v47, v34, s23
	v_and_or_b32 v34, v34, s95, v3
	v_bfe_u32 v3, v37, 16, 1
	v_add3_u32 v3, v37, v3, s23
	v_bfe_u32 v36, v35, 16, 1
	v_lshrrev_b32_e32 v3, 16, v3
	v_add3_u32 v35, v35, v36, s23
	v_and_or_b32 v35, v35, s95, v3
	v_bfe_u32 v3, v41, 16, 1
	v_add3_u32 v3, v41, v3, s23
	v_bfe_u32 v36, v39, 16, 1
	v_lshrrev_b32_e32 v3, 16, v3
	v_add3_u32 v36, v39, v36, s23
	v_and_or_b32 v36, v36, s95, v3
	v_bfe_u32 v3, v45, 16, 1
	v_add3_u32 v3, v45, v3, s23
	v_bfe_u32 v37, v43, 16, 1
	v_lshrrev_b32_e32 v3, 16, v3
	v_add3_u32 v37, v43, v37, s23
	v_and_or_b32 v37, v37, s95, v3
	v_lshl_add_u64 v[38:39], v[32:33], 0, v[26:27]
	global_store_dwordx4 v[56:57], v[52:55], off nt
	global_store_dwordx4 v[38:39], v[34:37], off nt
	ds_read2_b32 v[38:39], v50 offset0:49 offset1:57
	ds_read2_b32 v[40:41], v50 offset0:16 offset1:24
	ds_read2_b32 v[42:43], v50 offset0:82 offset1:90
	ds_read2_b32 v[44:45], v50 offset0:115 offset1:123
	ds_read2_b32 v[46:47], v50 offset0:148 offset1:156
	ds_read2_b32 v[48:49], v50 offset0:181 offset1:189
	ds_read2_b32 v[52:53], v50 offset0:214 offset1:222
	ds_read2_b32 v[54:55], v50 offset0:247 offset1:255
	s_waitcnt lgkmcnt(7)
	v_bfe_u32 v34, v38, 16, 1
	s_waitcnt lgkmcnt(6)
	v_bfe_u32 v3, v40, 16, 1
	v_add3_u32 v3, v40, v3, s23
	v_lshrrev_b32_e32 v3, 16, v3
	v_add3_u32 v34, v38, v34, s23
	v_and_or_b32 v34, v34, s95, v3
	s_waitcnt lgkmcnt(5)
	v_bfe_u32 v3, v42, 16, 1
	v_add3_u32 v3, v42, v3, s23
	s_waitcnt lgkmcnt(4)
	v_bfe_u32 v35, v44, 16, 1
	v_lshrrev_b32_e32 v3, 16, v3
	v_add3_u32 v35, v44, v35, s23
	v_and_or_b32 v35, v35, s95, v3
	s_waitcnt lgkmcnt(3)
	v_bfe_u32 v3, v46, 16, 1
	v_add3_u32 v3, v46, v3, s23
	s_waitcnt lgkmcnt(2)
	v_bfe_u32 v36, v48, 16, 1
	v_lshrrev_b32_e32 v3, 16, v3
	v_add3_u32 v36, v48, v36, s23
	v_and_or_b32 v36, v36, s95, v3
	s_waitcnt lgkmcnt(1)
	v_bfe_u32 v3, v52, 16, 1
	v_add3_u32 v3, v52, v3, s23
	s_waitcnt lgkmcnt(0)
	v_bfe_u32 v37, v54, 16, 1
	v_lshrrev_b32_e32 v3, 16, v3
	v_add3_u32 v37, v54, v37, s23
	v_and_or_b32 v37, v37, s95, v3
	v_lshl_add_u64 v[56:57], v[32:33], 0, v[28:29]
	v_bfe_u32 v3, v41, 16, 1
	global_store_dwordx4 v[56:57], v[34:37], off nt
	v_add3_u32 v3, v41, v3, s23
	v_lshrrev_b32_e32 v3, 16, v3
	v_bfe_u32 v34, v39, 16, 1
	v_add3_u32 v34, v39, v34, s23
	v_and_or_b32 v34, v34, s95, v3
	v_bfe_u32 v3, v43, 16, 1
	v_add3_u32 v3, v43, v3, s23
	v_bfe_u32 v35, v45, 16, 1
	v_lshrrev_b32_e32 v3, 16, v3
	v_add3_u32 v35, v45, v35, s23
	v_and_or_b32 v35, v35, s95, v3
	v_bfe_u32 v3, v47, 16, 1
	v_add3_u32 v3, v47, v3, s23
	v_bfe_u32 v36, v49, 16, 1
	v_lshrrev_b32_e32 v3, 16, v3
	v_add3_u32 v36, v49, v36, s23
	v_and_or_b32 v36, v36, s95, v3
	v_bfe_u32 v3, v53, 16, 1
	v_add3_u32 v3, v53, v3, s23
	v_bfe_u32 v37, v55, 16, 1
	v_lshrrev_b32_e32 v3, 16, v3
	v_add3_u32 v37, v55, v37, s23
	v_and_or_b32 v37, v37, s95, v3
	v_lshl_add_u64 v[32:33], v[32:33], 0, v[30:31]
	global_store_dwordx4 v[32:33], v[34:37], off nt
	s_waitcnt lgkmcnt(0)
	s_branch .LBB0_819
